# xor-16/xor-32 row-sum shuffles in the QKV and fused-norm epilogues done with v_permlane16/32_swap instead of ds_bpermute round trips
# baseline (speedup 1.0000x reference)
; __device__ __forceinline__ unsigned cvt_pk_bf16(float lo, float hi) { unsigned r; asm volatile("v_cvt_pk_bf16_f32 %0, %1, %2" : "=v"(r) : "v"(lo), "v"(hi)); return r; }
;     __device__ __forceinline__ void operator()(const f32x4 (&acc)[2][2][4][2], const Unit& u, int wr, int wc, int fr, int fq) const {
;         const int pn = u.ocol; int t, ldc, colt;
;         if (MODE == 0) { t = pn >> 2; ldc = 1024; colt = (pn & 3) * 256; }
;         else { if (pn < 4) { t = 0; ldc = 1024; colt = pn * 256; } else { t = pn - 3; ldc = 256; colt = 0; } }
;         bf16_t* base = Q + (size_t)t * stride; const float sc = (t == 0) ? scale0 : 1.f;
;         const int row0 = u.orow + wr * 64 + fr, col0 = colt + wc * 32 + 8 * fq;
; #pragma unroll
;         for (int ai = 0; ai < 2; ++ai)
; #pragma unroll
;             for (int m = 0; m < 4; ++m) { bf16_t* rowp = base + (size_t)(row0 + ai * HALF + m * 16) * ldc + col0;
; #pragma unroll
;                 for (int bj = 0; bj < 2; ++bj) { const f32x4 v0 = acc[ai][bj][m][0] * sc, v1 = acc[ai][bj][m][1] * sc;
;                     u32x4 w; w.x = cvt_pk_bf16(v0[0], v0[1]); w.y = cvt_pk_bf16(v0[2], v0[3]); w.z = cvt_pk_bf16(v1[0], v1[1]); w.w = cvt_pk_bf16(v1[2], v1[3]);
;                     *(u32x4*)(rowp + bj * HALF) = w;
;                     if (MODE == 0 && t < 2) { float ss = ((v0[0] * v0[0] + v0[1] * v0[1]) + (v0[2] * v0[2] + v0[3] * v0[3])) + ((v1[0] * v1[0] + v1[1] * v1[1]) + (v1[2] * v1[2] + v1[3] * v1[3]));
;                         ss += __shfl_xor(ss, 16); ss += __shfl_xor(ss, 32);
;                         if (fq == 0) nrm[(size_t)(t * 32 + 8 * (pn & 3) + 4 * bj + wc) * nrows + (row0 + ai * HALF + m * 16)] = ss; } } }
.LBB0_240:
	s_ashr_i32 s40, s12, 2
	s_ashr_i32 s41, s40, 31
	s_and_b32 s13, s12, 3
	s_lshl_b64 s[30:31], s[40:41], 25
	s_add_u32 s30, s38, s30
	s_addc_u32 s31, s39, s31
	s_cmp_lt_u32 s12, 4
	s_cselect_b64 vcc, -1, 0
	s_cmp_lt_i32 s40, 2
	v_add_u32_e32 v144, s59, v150
	v_lshl_add_u32 v140, s13, 8, v152
	s_cselect_b64 s[36:37], -1, 0
	s_lshl_b32 s12, s40, 5
	s_lshl_b32 s13, s13, 3
	v_ashrrev_i32_e32 v141, 31, v140
	s_or_b32 s12, s12, s13
	v_ashrrev_i32_e32 v145, 31, v144
	v_cndmask_b32_e32 v146, 1.0, v156, vcc
	v_lshl_add_u64 v[140:141], v[140:141], 1, s[30:31]
	s_or_b32 s30, s12, s49
	v_lshlrev_b64 v[142:143], 11, v[144:145]
	s_cmp_gt_i32 s40, 1
	v_lshl_add_u64 v[148:149], v[140:141], 0, v[142:143]
	v_pk_mul_f32 v[126:127], v[146:147], v[126:127] op_sel_hi:[0,1]
	v_pk_mul_f32 v[124:125], v[146:147], v[124:125] op_sel_hi:[0,1]
	v_pk_mul_f32 v[122:123], v[146:147], v[122:123] op_sel_hi:[0,1]
	v_pk_mul_f32 v[120:121], v[146:147], v[120:121] op_sel_hi:[0,1]
	v_cvt_pk_bf16_f32 v158, v124, v125
	v_cvt_pk_bf16_f32 v159, v126, v127
	v_cvt_pk_bf16_f32 v160, v120, v121
	v_cvt_pk_bf16_f32 v161, v122, v123
	global_store_dwordx4 v[148:149], v[158:161], off
	s_cbranch_scc1 .LBB0_244
	v_mul_f32_e32 v121, v121, v121
	v_fmac_f32_e32 v121, v120, v120
	v_mul_f32_e32 v120, v123, v123
	v_mul_f32_e32 v125, v125, v125
	v_fmac_f32_e32 v120, v122, v122
	v_and_b32_e32 v122, 64, v157
	v_fmac_f32_e32 v125, v124, v124
	v_mul_f32_e32 v124, v127, v127
	v_add_f32_e32 v120, v121, v120
	v_xor_b32_e32 v121, 16, v157
	v_add_u32_e32 v122, 64, v122
	v_fmac_f32_e32 v124, v126, v126
	v_cmp_lt_i32_e32 vcc, v121, v122
	v_add_f32_e32 v124, v125, v124
	v_add_f32_e32 v120, v124, v120
	v_cndmask_b32_e32 v121, v157, v121, vcc
	v_lshlrev_b32_e32 v121, 2, v121
	v_mov_b32_e32 v121, v120
	s_nop 1
	v_permlane16_swap_b32_e32 v121, v120
	s_waitcnt lgkmcnt(0)
	v_add_f32_e32 v120, v120, v121
	v_xor_b32_e32 v121, 32, v157
	v_cmp_lt_i32_e32 vcc, v121, v122
	s_nop 1
	v_cndmask_b32_e32 v121, v157, v121, vcc
	v_lshlrev_b32_e32 v121, 2, v121
	v_mov_b32_e32 v121, v120
	s_nop 1
	v_permlane32_swap_b32_e32 v121, v120
	s_and_saveexec_b64 s[12:13], s[8:9]
	s_cbranch_execz .LBB0_243
	s_ashr_i32 s31, s30, 31
	s_lshl_b64 s[40:41], s[30:31], 16
	s_add_u32 s40, s50, s40
	s_addc_u32 s41, s51, s41
	s_waitcnt lgkmcnt(0)
	v_add_f32_e32 v122, v120, v121
	v_lshl_add_u64 v[120:121], v[144:145], 2, s[40:41]
	global_store_dword v[120:121], v122, off

; __device__ __forceinline__ unsigned cvt_pk_bf16(float lo, float hi) { unsigned r; asm volatile("v_cvt_pk_bf16_f32 %0, %1, %2" : "=v"(r) : "v"(lo), "v"(hi)); return r; }
;     __device__ __forceinline__ void operator()(const f32x4 (&acc)[2][2][4][2], const Unit& u, int wr, int wc, int fr, int fq) const {
;     ...
;             for (int m = 0; m < 4; ++m) { bf16_t* rowp = base + (size_t)(row0 + ai * HALF + m * 16) * ldc + col0;
; #pragma unroll
;                 for (int bj = 0; bj < 2; ++bj) { const f32x4 v0 = acc[ai][bj][m][0] * sc, v1 = acc[ai][bj][m][1] * sc;
;                     u32x4 w; w.x = cvt_pk_bf16(v0[0], v0[1]); w.y = cvt_pk_bf16(v0[2], v0[3]); w.z = cvt_pk_bf16(v1[0], v1[1]); w.w = cvt_pk_bf16(v1[2], v1[3]);
;                     *(u32x4*)(rowp + bj * HALF) = w;
;                     if (MODE == 0 && t < 2) { float ss = ((v0[0] * v0[0] + v0[1] * v0[1]) + (v0[2] * v0[2] + v0[3] * v0[3])) + ((v1[0] * v1[0] + v1[1] * v1[1]) + (v1[2] * v1[2] + v1[3] * v1[3]));
;                         ss += __shfl_xor(ss, 16); ss += __shfl_xor(ss, 32);
;                         if (fq == 0) nrm[(size_t)(t * 32 + 8 * (pn & 3) + 4 * bj + wc) * nrows + (row0 + ai * HALF + m * 16)] = ss; } } }
.LBB0_244:
	v_mov_b32_e32 v147, v146
	v_mov_b32_e32 v120, v146
	s_waitcnt lgkmcnt(0)
	v_mov_b32_e32 v121, v146
	v_pk_mul_f32 v[116:117], v[146:147], v[116:117]
	v_pk_mul_f32 v[118:119], v[120:121], v[118:119]
	v_cvt_pk_bf16_f32 v122, v116, v117
	v_pk_mul_f32 v[114:115], v[120:121], v[114:115]
	v_pk_mul_f32 v[112:113], v[146:147], v[112:113]
	v_cvt_pk_bf16_f32 v123, v118, v119
	s_andn2_b64 vcc, exec, s[36:37]
	v_cvt_pk_bf16_f32 v124, v112, v113
	v_cvt_pk_bf16_f32 v125, v114, v115
	global_store_dwordx4 v[148:149], v[122:125], off offset:256
	s_nop 1
	v_cndmask_b32_e64 v122, 0, 1, s[36:37]
	v_cmp_ne_u32_e64 s[12:13], 1, v122
	s_cbranch_vccnz .LBB0_248
	v_mul_f32_e32 v113, v113, v113
	v_fmac_f32_e32 v113, v112, v112
	v_mul_f32_e32 v112, v115, v115
	v_mul_f32_e32 v117, v117, v117
	v_fmac_f32_e32 v112, v114, v114
	v_and_b32_e32 v114, 64, v157
	v_fmac_f32_e32 v117, v116, v116
	v_mul_f32_e32 v116, v119, v119
	v_add_f32_e32 v112, v113, v112
	v_xor_b32_e32 v113, 16, v157
	v_add_u32_e32 v114, 64, v114
	v_fmac_f32_e32 v116, v118, v118
	v_cmp_lt_i32_e32 vcc, v113, v114
	v_add_f32_e32 v116, v117, v116
	v_add_f32_e32 v112, v116, v112
	v_cndmask_b32_e32 v113, v157, v113, vcc
	v_lshlrev_b32_e32 v113, 2, v113
	v_mov_b32_e32 v113, v112
	s_nop 1
	v_permlane16_swap_b32_e32 v113, v112
	s_waitcnt lgkmcnt(0)
	v_add_f32_e32 v112, v112, v113
	v_xor_b32_e32 v113, 32, v157
	v_cmp_lt_i32_e32 vcc, v113, v114
	s_nop 1
	v_cndmask_b32_e32 v113, v157, v113, vcc
	v_lshlrev_b32_e32 v113, 2, v113
	v_mov_b32_e32 v113, v112
	s_nop 1
	v_permlane32_swap_b32_e32 v113, v112
	s_and_saveexec_b64 s[36:37], s[8:9]
	s_cbranch_execz .LBB0_247
	s_or_b32 s40, s30, 4
	s_ashr_i32 s41, s40, 31
	s_lshl_b64 s[40:41], s[40:41], 16
	s_add_u32 s40, s50, s40
	s_addc_u32 s41, s51, s41
	s_waitcnt lgkmcnt(0)
	v_add_f32_e32 v114, v112, v113
	v_lshl_add_u64 v[112:113], v[144:145], 2, s[40:41]
	global_store_dword v[112:113], v114, off

; __device__ __forceinline__ unsigned cvt_pk_bf16(float lo, float hi) { unsigned r; asm volatile("v_cvt_pk_bf16_f32 %0, %1, %2" : "=v"(r) : "v"(lo), "v"(hi)); return r; }
;     __device__ __forceinline__ void operator()(const f32x4 (&acc)[2][2][4][2], const Unit& u, int wr, int wc, int fr, int fq) const {
;     ...
;             for (int m = 0; m < 4; ++m) { bf16_t* rowp = base + (size_t)(row0 + ai * HALF + m * 16) * ldc + col0;
; #pragma unroll
;                 for (int bj = 0; bj < 2; ++bj) { const f32x4 v0 = acc[ai][bj][m][0] * sc, v1 = acc[ai][bj][m][1] * sc;
;                     u32x4 w; w.x = cvt_pk_bf16(v0[0], v0[1]); w.y = cvt_pk_bf16(v0[2], v0[3]); w.z = cvt_pk_bf16(v1[0], v1[1]); w.w = cvt_pk_bf16(v1[2], v1[3]);
;                     *(u32x4*)(rowp + bj * HALF) = w;
;                     if (MODE == 0 && t < 2) { float ss = ((v0[0] * v0[0] + v0[1] * v0[1]) + (v0[2] * v0[2] + v0[3] * v0[3])) + ((v1[0] * v1[0] + v1[1] * v1[1]) + (v1[2] * v1[2] + v1[3] * v1[3]));
;                         ss += __shfl_xor(ss, 16); ss += __shfl_xor(ss, 32);
;                         if (fq == 0) nrm[(size_t)(t * 32 + 8 * (pn & 3) + 4 * bj + wc) * nrows + (row0 + ai * HALF + m * 16)] = ss; } } }
.LBB0_248:
	v_add_co_u32_e32 v116, vcc, 0x8000, v148
	v_pk_mul_f32 v[110:111], v[120:121], v[110:111]
	s_nop 0
	v_addc_co_u32_e32 v117, vcc, 0, v149, vcc
	v_pk_mul_f32 v[108:109], v[146:147], v[108:109]
	v_pk_mul_f32 v[106:107], v[120:121], v[106:107]
	v_pk_mul_f32 v[104:105], v[146:147], v[104:105]
	s_and_b64 vcc, exec, s[12:13]
	v_cvt_pk_bf16_f32 v112, v108, v109
	s_waitcnt lgkmcnt(0)
	v_cvt_pk_bf16_f32 v113, v110, v111
	v_cvt_pk_bf16_f32 v114, v104, v105
	v_cvt_pk_bf16_f32 v115, v106, v107
	global_store_dwordx4 v[116:117], v[112:115], off
	s_cbranch_vccnz .LBB0_252
	v_mul_f32_e32 v105, v105, v105
	v_fmac_f32_e32 v105, v104, v104
	v_mul_f32_e32 v104, v107, v107
	v_mul_f32_e32 v109, v109, v109
	v_fmac_f32_e32 v104, v106, v106
	v_and_b32_e32 v106, 64, v157
	v_fmac_f32_e32 v109, v108, v108
	v_mul_f32_e32 v108, v111, v111
	v_add_f32_e32 v104, v105, v104
	v_xor_b32_e32 v105, 16, v157
	v_add_u32_e32 v106, 64, v106
	v_fmac_f32_e32 v108, v110, v110
	v_cmp_lt_i32_e32 vcc, v105, v106
	v_add_f32_e32 v108, v109, v108
	v_add_f32_e32 v104, v108, v104
	v_cndmask_b32_e32 v105, v157, v105, vcc
	v_lshlrev_b32_e32 v105, 2, v105
	v_mov_b32_e32 v105, v104
	s_nop 1
	v_permlane16_swap_b32_e32 v105, v104
	s_waitcnt lgkmcnt(0)
	v_add_f32_e32 v104, v104, v105
	v_xor_b32_e32 v105, 32, v157
	v_cmp_lt_i32_e32 vcc, v105, v106
	s_nop 1
	v_cndmask_b32_e32 v105, v157, v105, vcc
	v_lshlrev_b32_e32 v105, 2, v105
	v_mov_b32_e32 v105, v104
	s_nop 1
	v_permlane32_swap_b32_e32 v105, v104
	s_and_saveexec_b64 s[36:37], s[8:9]
	s_cbranch_execz .LBB0_251
	s_ashr_i32 s31, s30, 31
	s_lshl_b64 s[40:41], s[30:31], 16
	s_add_u32 s40, s50, s40
	s_addc_u32 s41, s51, s41
	s_waitcnt lgkmcnt(0)
	v_add_f32_e32 v106, v104, v105
	v_lshl_add_u64 v[104:105], v[144:145], 2, s[40:41]
	global_store_dword v[104:105], v106, off offset:64

; __device__ __forceinline__ unsigned cvt_pk_bf16(float lo, float hi) { unsigned r; asm volatile("v_cvt_pk_bf16_f32 %0, %1, %2" : "=v"(r) : "v"(lo), "v"(hi)); return r; }
;     __device__ __forceinline__ void operator()(const f32x4 (&acc)[2][2][4][2], const Unit& u, int wr, int wc, int fr, int fq) const {
;     ...
;             for (int m = 0; m < 4; ++m) { bf16_t* rowp = base + (size_t)(row0 + ai * HALF + m * 16) * ldc + col0;
; #pragma unroll
;                 for (int bj = 0; bj < 2; ++bj) { const f32x4 v0 = acc[ai][bj][m][0] * sc, v1 = acc[ai][bj][m][1] * sc;
;                     u32x4 w; w.x = cvt_pk_bf16(v0[0], v0[1]); w.y = cvt_pk_bf16(v0[2], v0[3]); w.z = cvt_pk_bf16(v1[0], v1[1]); w.w = cvt_pk_bf16(v1[2], v1[3]);
;                     *(u32x4*)(rowp + bj * HALF) = w;
;                     if (MODE == 0 && t < 2) { float ss = ((v0[0] * v0[0] + v0[1] * v0[1]) + (v0[2] * v0[2] + v0[3] * v0[3])) + ((v1[0] * v1[0] + v1[1] * v1[1]) + (v1[2] * v1[2] + v1[3] * v1[3]));
;                         ss += __shfl_xor(ss, 16); ss += __shfl_xor(ss, 32);
;                         if (fq == 0) nrm[(size_t)(t * 32 + 8 * (pn & 3) + 4 * bj + wc) * nrows + (row0 + ai * HALF + m * 16)] = ss; } } }
.LBB0_252:
	s_mov_b64 s[36:37], 0x8000
	v_mov_b32_e32 v104, v146
	s_waitcnt lgkmcnt(0)
	v_mov_b32_e32 v105, v146
	v_lshl_add_u64 v[110:111], v[148:149], 0, s[36:37]
	v_pk_mul_f32 v[102:103], v[104:105], v[102:103]
	v_pk_mul_f32 v[100:101], v[146:147], v[100:101]
	v_pk_mul_f32 v[98:99], v[104:105], v[98:99]
	v_pk_mul_f32 v[96:97], v[146:147], v[96:97]
	s_and_b64 vcc, exec, s[12:13]
	v_cvt_pk_bf16_f32 v106, v100, v101
	v_cvt_pk_bf16_f32 v107, v102, v103
	v_cvt_pk_bf16_f32 v108, v96, v97
	v_cvt_pk_bf16_f32 v109, v98, v99
	global_store_dwordx4 v[110:111], v[106:109], off offset:256
	s_cbranch_vccnz .LBB0_256
	v_mul_f32_e32 v97, v97, v97
	v_fmac_f32_e32 v97, v96, v96
	v_mul_f32_e32 v96, v99, v99
	v_mul_f32_e32 v101, v101, v101
	v_fmac_f32_e32 v96, v98, v98
	v_and_b32_e32 v98, 64, v157
	v_fmac_f32_e32 v101, v100, v100
	v_mul_f32_e32 v100, v103, v103
	v_add_f32_e32 v96, v97, v96
	v_xor_b32_e32 v97, 16, v157
	v_add_u32_e32 v98, 64, v98
	v_fmac_f32_e32 v100, v102, v102
	v_cmp_lt_i32_e32 vcc, v97, v98
	v_add_f32_e32 v100, v101, v100
	v_add_f32_e32 v96, v100, v96
	v_cndmask_b32_e32 v97, v157, v97, vcc
	v_lshlrev_b32_e32 v97, 2, v97
	v_mov_b32_e32 v97, v96
	s_nop 1
	v_permlane16_swap_b32_e32 v97, v96
	s_waitcnt lgkmcnt(0)
	v_add_f32_e32 v96, v96, v97
	v_xor_b32_e32 v97, 32, v157
	v_cmp_lt_i32_e32 vcc, v97, v98
	s_nop 1
	v_cndmask_b32_e32 v97, v157, v97, vcc
	v_lshlrev_b32_e32 v97, 2, v97
	v_mov_b32_e32 v97, v96
	s_nop 1
	v_permlane32_swap_b32_e32 v97, v96
	s_and_saveexec_b64 s[36:37], s[8:9]
	s_cbranch_execz .LBB0_255
	s_or_b32 s40, s30, 4
	s_ashr_i32 s41, s40, 31
	s_lshl_b64 s[40:41], s[40:41], 16
	s_add_u32 s40, s50, s40
	s_addc_u32 s41, s51, s41
	s_waitcnt lgkmcnt(0)
	v_add_f32_e32 v98, v96, v97
	v_lshl_add_u64 v[96:97], v[144:145], 2, s[40:41]
	global_store_dword v[96:97], v98, off offset:64

; __device__ __forceinline__ unsigned cvt_pk_bf16(float lo, float hi) { unsigned r; asm volatile("v_cvt_pk_bf16_f32 %0, %1, %2" : "=v"(r) : "v"(lo), "v"(hi)); return r; }
;     __device__ __forceinline__ void operator()(const f32x4 (&acc)[2][2][4][2], const Unit& u, int wr, int wc, int fr, int fq) const {
;     ...
;             for (int m = 0; m < 4; ++m) { bf16_t* rowp = base + (size_t)(row0 + ai * HALF + m * 16) * ldc + col0;
; #pragma unroll
;                 for (int bj = 0; bj < 2; ++bj) { const f32x4 v0 = acc[ai][bj][m][0] * sc, v1 = acc[ai][bj][m][1] * sc;
;                     u32x4 w; w.x = cvt_pk_bf16(v0[0], v0[1]); w.y = cvt_pk_bf16(v0[2], v0[3]); w.z = cvt_pk_bf16(v1[0], v1[1]); w.w = cvt_pk_bf16(v1[2], v1[3]);
;                     *(u32x4*)(rowp + bj * HALF) = w;
;                     if (MODE == 0 && t < 2) { float ss = ((v0[0] * v0[0] + v0[1] * v0[1]) + (v0[2] * v0[2] + v0[3] * v0[3])) + ((v1[0] * v1[0] + v1[1] * v1[1]) + (v1[2] * v1[2] + v1[3] * v1[3]));
;                         ss += __shfl_xor(ss, 16); ss += __shfl_xor(ss, 32);
;                         if (fq == 0) nrm[(size_t)(t * 32 + 8 * (pn & 3) + 4 * bj + wc) * nrows + (row0 + ai * HALF + m * 16)] = ss; } } }
.LBB0_256:
	v_add_co_u32_e32 v100, vcc, 0x10000, v148
	v_pk_mul_f32 v[94:95], v[104:105], v[94:95]
	s_nop 0
	v_addc_co_u32_e32 v101, vcc, 0, v149, vcc
	v_pk_mul_f32 v[92:93], v[146:147], v[92:93]
	v_pk_mul_f32 v[90:91], v[104:105], v[90:91]
	v_pk_mul_f32 v[88:89], v[146:147], v[88:89]
	s_and_b64 vcc, exec, s[12:13]
	v_cvt_pk_bf16_f32 v96, v92, v93
	s_waitcnt lgkmcnt(0)
	v_cvt_pk_bf16_f32 v97, v94, v95
	v_cvt_pk_bf16_f32 v98, v88, v89
	v_cvt_pk_bf16_f32 v99, v90, v91
	global_store_dwordx4 v[100:101], v[96:99], off
	s_cbranch_vccnz .LBB0_260
	v_mul_f32_e32 v89, v89, v89
	v_fmac_f32_e32 v89, v88, v88
	v_mul_f32_e32 v88, v91, v91
	v_mul_f32_e32 v93, v93, v93
	v_fmac_f32_e32 v88, v90, v90
	v_and_b32_e32 v90, 64, v157
	v_fmac_f32_e32 v93, v92, v92
	v_mul_f32_e32 v92, v95, v95
	v_add_f32_e32 v88, v89, v88
	v_xor_b32_e32 v89, 16, v157
	v_add_u32_e32 v90, 64, v90
	v_fmac_f32_e32 v92, v94, v94
	v_cmp_lt_i32_e32 vcc, v89, v90
	v_add_f32_e32 v92, v93, v92
	v_add_f32_e32 v88, v92, v88
	v_cndmask_b32_e32 v89, v157, v89, vcc
	v_lshlrev_b32_e32 v89, 2, v89
	v_mov_b32_e32 v89, v88
	s_nop 1
	v_permlane16_swap_b32_e32 v89, v88
	s_waitcnt lgkmcnt(0)
	v_add_f32_e32 v88, v88, v89
	v_xor_b32_e32 v89, 32, v157
	v_cmp_lt_i32_e32 vcc, v89, v90
	s_nop 1
	v_cndmask_b32_e32 v89, v157, v89, vcc
	v_lshlrev_b32_e32 v89, 2, v89
	v_mov_b32_e32 v89, v88
	s_nop 1
	v_permlane32_swap_b32_e32 v89, v88
	s_and_saveexec_b64 s[36:37], s[8:9]
	s_cbranch_execz .LBB0_259
	s_ashr_i32 s31, s30, 31
	s_lshl_b64 s[40:41], s[30:31], 16
	s_add_u32 s40, s50, s40
	s_addc_u32 s41, s51, s41
	s_waitcnt lgkmcnt(0)
	v_add_f32_e32 v90, v88, v89
	v_lshl_add_u64 v[88:89], v[144:145], 2, s[40:41]
	global_store_dword v[88:89], v90, off offset:128

; __device__ __forceinline__ unsigned cvt_pk_bf16(float lo, float hi) { unsigned r; asm volatile("v_cvt_pk_bf16_f32 %0, %1, %2" : "=v"(r) : "v"(lo), "v"(hi)); return r; }
;     __device__ __forceinline__ void operator()(const f32x4 (&acc)[2][2][4][2], const Unit& u, int wr, int wc, int fr, int fq) const {
;     ...
;             for (int m = 0; m < 4; ++m) { bf16_t* rowp = base + (size_t)(row0 + ai * HALF + m * 16) * ldc + col0;
; #pragma unroll
;                 for (int bj = 0; bj < 2; ++bj) { const f32x4 v0 = acc[ai][bj][m][0] * sc, v1 = acc[ai][bj][m][1] * sc;
;                     u32x4 w; w.x = cvt_pk_bf16(v0[0], v0[1]); w.y = cvt_pk_bf16(v0[2], v0[3]); w.z = cvt_pk_bf16(v1[0], v1[1]); w.w = cvt_pk_bf16(v1[2], v1[3]);
;                     *(u32x4*)(rowp + bj * HALF) = w;
;                     if (MODE == 0 && t < 2) { float ss = ((v0[0] * v0[0] + v0[1] * v0[1]) + (v0[2] * v0[2] + v0[3] * v0[3])) + ((v1[0] * v1[0] + v1[1] * v1[1]) + (v1[2] * v1[2] + v1[3] * v1[3]));
;                         ss += __shfl_xor(ss, 16); ss += __shfl_xor(ss, 32);
;                         if (fq == 0) nrm[(size_t)(t * 32 + 8 * (pn & 3) + 4 * bj + wc) * nrows + (row0 + ai * HALF + m * 16)] = ss; } } }
.LBB0_260:
	s_mov_b64 s[36:37], 0x10000
	v_mov_b32_e32 v88, v146
	s_waitcnt lgkmcnt(0)
	v_mov_b32_e32 v89, v146
	v_lshl_add_u64 v[94:95], v[148:149], 0, s[36:37]
	v_pk_mul_f32 v[86:87], v[88:89], v[86:87]
	v_pk_mul_f32 v[84:85], v[146:147], v[84:85]
	v_pk_mul_f32 v[82:83], v[88:89], v[82:83]
	v_pk_mul_f32 v[80:81], v[146:147], v[80:81]
	s_and_b64 vcc, exec, s[12:13]
	v_cvt_pk_bf16_f32 v90, v84, v85
	v_cvt_pk_bf16_f32 v91, v86, v87
	v_cvt_pk_bf16_f32 v92, v80, v81
	v_cvt_pk_bf16_f32 v93, v82, v83
	global_store_dwordx4 v[94:95], v[90:93], off offset:256
	s_cbranch_vccnz .LBB0_264
	v_mul_f32_e32 v81, v81, v81
	v_fmac_f32_e32 v81, v80, v80
	v_mul_f32_e32 v80, v83, v83
	v_mul_f32_e32 v85, v85, v85
	v_fmac_f32_e32 v80, v82, v82
	v_and_b32_e32 v82, 64, v157
	v_fmac_f32_e32 v85, v84, v84
	v_mul_f32_e32 v84, v87, v87
	v_add_f32_e32 v80, v81, v80
	v_xor_b32_e32 v81, 16, v157
	v_add_u32_e32 v82, 64, v82
	v_fmac_f32_e32 v84, v86, v86
	v_cmp_lt_i32_e32 vcc, v81, v82
	v_add_f32_e32 v84, v85, v84
	v_add_f32_e32 v80, v84, v80
	v_cndmask_b32_e32 v81, v157, v81, vcc
	v_lshlrev_b32_e32 v81, 2, v81
	v_mov_b32_e32 v81, v80
	s_nop 1
	v_permlane16_swap_b32_e32 v81, v80
	s_waitcnt lgkmcnt(0)
	v_add_f32_e32 v80, v80, v81
	v_xor_b32_e32 v81, 32, v157
	v_cmp_lt_i32_e32 vcc, v81, v82
	s_nop 1
	v_cndmask_b32_e32 v81, v157, v81, vcc
	v_lshlrev_b32_e32 v81, 2, v81
	v_mov_b32_e32 v81, v80
	s_nop 1
	v_permlane32_swap_b32_e32 v81, v80
	s_and_saveexec_b64 s[36:37], s[8:9]
	s_cbranch_execz .LBB0_263
	s_or_b32 s40, s30, 4
	s_ashr_i32 s41, s40, 31
	s_lshl_b64 s[40:41], s[40:41], 16
	s_add_u32 s40, s50, s40
	s_addc_u32 s41, s51, s41
	s_waitcnt lgkmcnt(0)
	v_add_f32_e32 v82, v80, v81
	v_lshl_add_u64 v[80:81], v[144:145], 2, s[40:41]
	global_store_dword v[80:81], v82, off offset:128

; __device__ __forceinline__ unsigned cvt_pk_bf16(float lo, float hi) { unsigned r; asm volatile("v_cvt_pk_bf16_f32 %0, %1, %2" : "=v"(r) : "v"(lo), "v"(hi)); return r; }
;     __device__ __forceinline__ void operator()(const f32x4 (&acc)[2][2][4][2], const Unit& u, int wr, int wc, int fr, int fq) const {
;     ...
;             for (int m = 0; m < 4; ++m) { bf16_t* rowp = base + (size_t)(row0 + ai * HALF + m * 16) * ldc + col0;
; #pragma unroll
;                 for (int bj = 0; bj < 2; ++bj) { const f32x4 v0 = acc[ai][bj][m][0] * sc, v1 = acc[ai][bj][m][1] * sc;
;                     u32x4 w; w.x = cvt_pk_bf16(v0[0], v0[1]); w.y = cvt_pk_bf16(v0[2], v0[3]); w.z = cvt_pk_bf16(v1[0], v1[1]); w.w = cvt_pk_bf16(v1[2], v1[3]);
;                     *(u32x4*)(rowp + bj * HALF) = w;
;                     if (MODE == 0 && t < 2) { float ss = ((v0[0] * v0[0] + v0[1] * v0[1]) + (v0[2] * v0[2] + v0[3] * v0[3])) + ((v1[0] * v1[0] + v1[1] * v1[1]) + (v1[2] * v1[2] + v1[3] * v1[3]));
;                         ss += __shfl_xor(ss, 16); ss += __shfl_xor(ss, 32);
;                         if (fq == 0) nrm[(size_t)(t * 32 + 8 * (pn & 3) + 4 * bj + wc) * nrows + (row0 + ai * HALF + m * 16)] = ss; } } }
.LBB0_264:
	v_add_co_u32_e32 v84, vcc, 0x18000, v148
	v_pk_mul_f32 v[78:79], v[88:89], v[78:79]
	s_nop 0
	v_addc_co_u32_e32 v85, vcc, 0, v149, vcc
	v_pk_mul_f32 v[76:77], v[146:147], v[76:77]
	v_pk_mul_f32 v[74:75], v[88:89], v[74:75]
	v_pk_mul_f32 v[72:73], v[146:147], v[72:73]
	s_and_b64 vcc, exec, s[12:13]
	v_cvt_pk_bf16_f32 v80, v76, v77
	s_waitcnt lgkmcnt(0)
	v_cvt_pk_bf16_f32 v81, v78, v79
	v_cvt_pk_bf16_f32 v82, v72, v73
	v_cvt_pk_bf16_f32 v83, v74, v75
	global_store_dwordx4 v[84:85], v[80:83], off
	s_cbranch_vccnz .LBB0_268
	v_mul_f32_e32 v73, v73, v73
	v_fmac_f32_e32 v73, v72, v72
	v_mul_f32_e32 v72, v75, v75
	v_mul_f32_e32 v77, v77, v77
	v_fmac_f32_e32 v72, v74, v74
	v_and_b32_e32 v74, 64, v157
	v_fmac_f32_e32 v77, v76, v76
	v_mul_f32_e32 v76, v79, v79
	v_add_f32_e32 v72, v73, v72
	v_xor_b32_e32 v73, 16, v157
	v_add_u32_e32 v74, 64, v74
	v_fmac_f32_e32 v76, v78, v78
	v_cmp_lt_i32_e32 vcc, v73, v74
	v_add_f32_e32 v76, v77, v76
	v_add_f32_e32 v72, v76, v72
	v_cndmask_b32_e32 v73, v157, v73, vcc
	v_lshlrev_b32_e32 v73, 2, v73
	v_mov_b32_e32 v73, v72
	s_nop 1
	v_permlane16_swap_b32_e32 v73, v72
	s_waitcnt lgkmcnt(0)
	v_add_f32_e32 v72, v72, v73
	v_xor_b32_e32 v73, 32, v157
	v_cmp_lt_i32_e32 vcc, v73, v74
	s_nop 1
	v_cndmask_b32_e32 v73, v157, v73, vcc
	v_lshlrev_b32_e32 v73, 2, v73
	v_mov_b32_e32 v73, v72
	s_nop 1
	v_permlane32_swap_b32_e32 v73, v72
	s_and_saveexec_b64 s[36:37], s[8:9]
	s_cbranch_execz .LBB0_267
	s_ashr_i32 s31, s30, 31
	s_lshl_b64 s[40:41], s[30:31], 16
	s_add_u32 s40, s50, s40
	s_addc_u32 s41, s51, s41
	s_waitcnt lgkmcnt(0)
	v_add_f32_e32 v74, v72, v73
	v_lshl_add_u64 v[72:73], v[144:145], 2, s[40:41]
	global_store_dword v[72:73], v74, off offset:192

; __device__ __forceinline__ unsigned cvt_pk_bf16(float lo, float hi) { unsigned r; asm volatile("v_cvt_pk_bf16_f32 %0, %1, %2" : "=v"(r) : "v"(lo), "v"(hi)); return r; }
;     __device__ __forceinline__ void operator()(const f32x4 (&acc)[2][2][4][2], const Unit& u, int wr, int wc, int fr, int fq) const {
;     ...
;             for (int m = 0; m < 4; ++m) { bf16_t* rowp = base + (size_t)(row0 + ai * HALF + m * 16) * ldc + col0;
; #pragma unroll
;                 for (int bj = 0; bj < 2; ++bj) { const f32x4 v0 = acc[ai][bj][m][0] * sc, v1 = acc[ai][bj][m][1] * sc;
;                     u32x4 w; w.x = cvt_pk_bf16(v0[0], v0[1]); w.y = cvt_pk_bf16(v0[2], v0[3]); w.z = cvt_pk_bf16(v1[0], v1[1]); w.w = cvt_pk_bf16(v1[2], v1[3]);
;                     *(u32x4*)(rowp + bj * HALF) = w;
;                     if (MODE == 0 && t < 2) { float ss = ((v0[0] * v0[0] + v0[1] * v0[1]) + (v0[2] * v0[2] + v0[3] * v0[3])) + ((v1[0] * v1[0] + v1[1] * v1[1]) + (v1[2] * v1[2] + v1[3] * v1[3]));
;                         ss += __shfl_xor(ss, 16); ss += __shfl_xor(ss, 32);
;                         if (fq == 0) nrm[(size_t)(t * 32 + 8 * (pn & 3) + 4 * bj + wc) * nrows + (row0 + ai * HALF + m * 16)] = ss; } } }
.LBB0_268:
	s_mov_b64 s[36:37], 0x18000
	v_mov_b32_e32 v72, v146
	s_waitcnt lgkmcnt(0)
	v_mov_b32_e32 v73, v146
	v_lshl_add_u64 v[78:79], v[148:149], 0, s[36:37]
	v_pk_mul_f32 v[70:71], v[72:73], v[70:71]
	v_pk_mul_f32 v[68:69], v[146:147], v[68:69]
	v_pk_mul_f32 v[66:67], v[72:73], v[66:67]
	v_pk_mul_f32 v[64:65], v[146:147], v[64:65]
	s_and_b64 vcc, exec, s[12:13]
	v_cvt_pk_bf16_f32 v74, v68, v69
	v_cvt_pk_bf16_f32 v75, v70, v71
	v_cvt_pk_bf16_f32 v76, v64, v65
	v_cvt_pk_bf16_f32 v77, v66, v67
	global_store_dwordx4 v[78:79], v[74:77], off offset:256
	s_cbranch_vccnz .LBB0_272
	v_mul_f32_e32 v65, v65, v65
	v_fmac_f32_e32 v65, v64, v64
	v_mul_f32_e32 v64, v67, v67
	v_mul_f32_e32 v69, v69, v69
	v_fmac_f32_e32 v64, v66, v66
	v_and_b32_e32 v66, 64, v157
	v_fmac_f32_e32 v69, v68, v68
	v_mul_f32_e32 v68, v71, v71
	v_add_f32_e32 v64, v65, v64
	v_xor_b32_e32 v65, 16, v157
	v_add_u32_e32 v66, 64, v66
	v_fmac_f32_e32 v68, v70, v70
	v_cmp_lt_i32_e32 vcc, v65, v66
	v_add_f32_e32 v68, v69, v68
	v_add_f32_e32 v64, v68, v64
	v_cndmask_b32_e32 v65, v157, v65, vcc
	v_lshlrev_b32_e32 v65, 2, v65
	v_mov_b32_e32 v65, v64
	s_nop 1
	v_permlane16_swap_b32_e32 v65, v64
	s_waitcnt lgkmcnt(0)
	v_add_f32_e32 v64, v64, v65
	v_xor_b32_e32 v65, 32, v157
	v_cmp_lt_i32_e32 vcc, v65, v66
	s_nop 1
	v_cndmask_b32_e32 v65, v157, v65, vcc
	v_lshlrev_b32_e32 v65, 2, v65
	v_mov_b32_e32 v65, v64
	s_nop 1
	v_permlane32_swap_b32_e32 v65, v64
	s_and_saveexec_b64 s[36:37], s[8:9]
	s_cbranch_execz .LBB0_271
	s_or_b32 s40, s30, 4
	s_ashr_i32 s41, s40, 31
	s_lshl_b64 s[40:41], s[40:41], 16
	s_add_u32 s40, s50, s40
	s_addc_u32 s41, s51, s41
	s_waitcnt lgkmcnt(0)
	v_add_f32_e32 v66, v64, v65
	v_lshl_add_u64 v[64:65], v[144:145], 2, s[40:41]
	global_store_dword v[64:65], v66, off offset:192

; __device__ __forceinline__ unsigned cvt_pk_bf16(float lo, float hi) { unsigned r; asm volatile("v_cvt_pk_bf16_f32 %0, %1, %2" : "=v"(r) : "v"(lo), "v"(hi)); return r; }
;     __device__ __forceinline__ void operator()(const f32x4 (&acc)[2][2][4][2], const Unit& u, int wr, int wc, int fr, int fq) const {
;     ...
;             for (int m = 0; m < 4; ++m) { bf16_t* rowp = base + (size_t)(row0 + ai * HALF + m * 16) * ldc + col0;
; #pragma unroll
;                 for (int bj = 0; bj < 2; ++bj) { const f32x4 v0 = acc[ai][bj][m][0] * sc, v1 = acc[ai][bj][m][1] * sc;
;                     u32x4 w; w.x = cvt_pk_bf16(v0[0], v0[1]); w.y = cvt_pk_bf16(v0[2], v0[3]); w.z = cvt_pk_bf16(v1[0], v1[1]); w.w = cvt_pk_bf16(v1[2], v1[3]);
;                     *(u32x4*)(rowp + bj * HALF) = w;
;                     if (MODE == 0 && t < 2) { float ss = ((v0[0] * v0[0] + v0[1] * v0[1]) + (v0[2] * v0[2] + v0[3] * v0[3])) + ((v1[0] * v1[0] + v1[1] * v1[1]) + (v1[2] * v1[2] + v1[3] * v1[3]));
;                         ss += __shfl_xor(ss, 16); ss += __shfl_xor(ss, 32);
;                         if (fq == 0) nrm[(size_t)(t * 32 + 8 * (pn & 3) + 4 * bj + wc) * nrows + (row0 + ai * HALF + m * 16)] = ss; } } }
.LBB0_272:
	v_add_co_u32_e32 v68, vcc, 0x40000, v148
	v_pk_mul_f32 v[62:63], v[72:73], v[62:63]
	s_nop 0
	v_addc_co_u32_e32 v69, vcc, 0, v149, vcc
	v_pk_mul_f32 v[60:61], v[146:147], v[60:61]
	v_pk_mul_f32 v[58:59], v[72:73], v[58:59]
	v_pk_mul_f32 v[56:57], v[146:147], v[56:57]
	s_and_b64 vcc, exec, s[12:13]
	v_cvt_pk_bf16_f32 v64, v60, v61
	s_waitcnt lgkmcnt(0)
	v_cvt_pk_bf16_f32 v65, v62, v63
	v_cvt_pk_bf16_f32 v66, v56, v57
	v_cvt_pk_bf16_f32 v67, v58, v59
	global_store_dwordx4 v[68:69], v[64:67], off
	s_cbranch_vccnz .LBB0_276
	v_mul_f32_e32 v57, v57, v57
	v_fmac_f32_e32 v57, v56, v56
	v_mul_f32_e32 v56, v59, v59
	v_mul_f32_e32 v61, v61, v61
	v_fmac_f32_e32 v56, v58, v58
	v_and_b32_e32 v58, 64, v157
	v_fmac_f32_e32 v61, v60, v60
	v_mul_f32_e32 v60, v63, v63
	v_add_f32_e32 v56, v57, v56
	v_xor_b32_e32 v57, 16, v157
	v_add_u32_e32 v58, 64, v58
	v_fmac_f32_e32 v60, v62, v62
	v_cmp_lt_i32_e32 vcc, v57, v58
	v_add_f32_e32 v60, v61, v60
	v_add_f32_e32 v56, v60, v56
	v_cndmask_b32_e32 v57, v157, v57, vcc
	v_lshlrev_b32_e32 v57, 2, v57
	v_mov_b32_e32 v57, v56
	s_nop 1
	v_permlane16_swap_b32_e32 v57, v56
	s_waitcnt lgkmcnt(0)
	v_add_f32_e32 v56, v56, v57
	v_xor_b32_e32 v57, 32, v157
	v_cmp_lt_i32_e32 vcc, v57, v58
	s_nop 1
	v_cndmask_b32_e32 v57, v157, v57, vcc
	v_lshlrev_b32_e32 v57, 2, v57
	v_mov_b32_e32 v57, v56
	s_nop 1
	v_permlane32_swap_b32_e32 v57, v56
	s_and_saveexec_b64 s[36:37], s[8:9]
	s_cbranch_execz .LBB0_275
	s_ashr_i32 s31, s30, 31
	s_lshl_b64 s[40:41], s[30:31], 16
	s_add_u32 s40, s50, s40
	s_addc_u32 s41, s51, s41
	s_waitcnt lgkmcnt(0)
	v_add_f32_e32 v58, v56, v57
	v_lshl_add_u64 v[56:57], v[144:145], 2, s[40:41]
	global_store_dword v[56:57], v58, off offset:512

; __device__ __forceinline__ unsigned cvt_pk_bf16(float lo, float hi) { unsigned r; asm volatile("v_cvt_pk_bf16_f32 %0, %1, %2" : "=v"(r) : "v"(lo), "v"(hi)); return r; }
;     __device__ __forceinline__ void operator()(const f32x4 (&acc)[2][2][4][2], const Unit& u, int wr, int wc, int fr, int fq) const {
;     ...
;             for (int m = 0; m < 4; ++m) { bf16_t* rowp = base + (size_t)(row0 + ai * HALF + m * 16) * ldc + col0;
; #pragma unroll
;                 for (int bj = 0; bj < 2; ++bj) { const f32x4 v0 = acc[ai][bj][m][0] * sc, v1 = acc[ai][bj][m][1] * sc;
;                     u32x4 w; w.x = cvt_pk_bf16(v0[0], v0[1]); w.y = cvt_pk_bf16(v0[2], v0[3]); w.z = cvt_pk_bf16(v1[0], v1[1]); w.w = cvt_pk_bf16(v1[2], v1[3]);
;                     *(u32x4*)(rowp + bj * HALF) = w;
;                     if (MODE == 0 && t < 2) { float ss = ((v0[0] * v0[0] + v0[1] * v0[1]) + (v0[2] * v0[2] + v0[3] * v0[3])) + ((v1[0] * v1[0] + v1[1] * v1[1]) + (v1[2] * v1[2] + v1[3] * v1[3]));
;                         ss += __shfl_xor(ss, 16); ss += __shfl_xor(ss, 32);
;                         if (fq == 0) nrm[(size_t)(t * 32 + 8 * (pn & 3) + 4 * bj + wc) * nrows + (row0 + ai * HALF + m * 16)] = ss; } } }
.LBB0_276:
	s_mov_b64 s[36:37], 0x40000
	v_mov_b32_e32 v56, v146
	s_waitcnt lgkmcnt(0)
	v_mov_b32_e32 v57, v146
	v_lshl_add_u64 v[62:63], v[148:149], 0, s[36:37]
	v_pk_mul_f32 v[54:55], v[56:57], v[54:55]
	v_pk_mul_f32 v[52:53], v[146:147], v[52:53]
	v_pk_mul_f32 v[50:51], v[56:57], v[50:51]
	v_pk_mul_f32 v[48:49], v[146:147], v[48:49]
	s_and_b64 vcc, exec, s[12:13]
	v_cvt_pk_bf16_f32 v58, v52, v53
	v_cvt_pk_bf16_f32 v59, v54, v55
	v_cvt_pk_bf16_f32 v60, v48, v49
	v_cvt_pk_bf16_f32 v61, v50, v51
	global_store_dwordx4 v[62:63], v[58:61], off offset:256
	s_cbranch_vccnz .LBB0_280
	v_mul_f32_e32 v49, v49, v49
	v_fmac_f32_e32 v49, v48, v48
	v_mul_f32_e32 v48, v51, v51
	v_mul_f32_e32 v53, v53, v53
	v_fmac_f32_e32 v48, v50, v50
	v_and_b32_e32 v50, 64, v157
	v_fmac_f32_e32 v53, v52, v52
	v_mul_f32_e32 v52, v55, v55
	v_add_f32_e32 v48, v49, v48
	v_xor_b32_e32 v49, 16, v157
	v_add_u32_e32 v50, 64, v50
	v_fmac_f32_e32 v52, v54, v54
	v_cmp_lt_i32_e32 vcc, v49, v50
	v_add_f32_e32 v52, v53, v52
	v_add_f32_e32 v48, v52, v48
	v_cndmask_b32_e32 v49, v157, v49, vcc
	v_lshlrev_b32_e32 v49, 2, v49
	v_mov_b32_e32 v49, v48
	s_nop 1
	v_permlane16_swap_b32_e32 v49, v48
	s_waitcnt lgkmcnt(0)
	v_add_f32_e32 v48, v48, v49
	v_xor_b32_e32 v49, 32, v157
	v_cmp_lt_i32_e32 vcc, v49, v50
	s_nop 1
	v_cndmask_b32_e32 v49, v157, v49, vcc
	v_lshlrev_b32_e32 v49, 2, v49
	v_mov_b32_e32 v49, v48
	s_nop 1
	v_permlane32_swap_b32_e32 v49, v48
	s_and_saveexec_b64 s[36:37], s[8:9]
	s_cbranch_execz .LBB0_279
	s_or_b32 s40, s30, 4
	s_ashr_i32 s41, s40, 31
	s_lshl_b64 s[40:41], s[40:41], 16
	s_add_u32 s40, s50, s40
	s_addc_u32 s41, s51, s41
	s_waitcnt lgkmcnt(0)
	v_add_f32_e32 v50, v48, v49
	v_lshl_add_u64 v[48:49], v[144:145], 2, s[40:41]
	global_store_dword v[48:49], v50, off offset:512

; __device__ __forceinline__ unsigned cvt_pk_bf16(float lo, float hi) { unsigned r; asm volatile("v_cvt_pk_bf16_f32 %0, %1, %2" : "=v"(r) : "v"(lo), "v"(hi)); return r; }
;     __device__ __forceinline__ void operator()(const f32x4 (&acc)[2][2][4][2], const Unit& u, int wr, int wc, int fr, int fq) const {
;     ...
;             for (int m = 0; m < 4; ++m) { bf16_t* rowp = base + (size_t)(row0 + ai * HALF + m * 16) * ldc + col0;
; #pragma unroll
;                 for (int bj = 0; bj < 2; ++bj) { const f32x4 v0 = acc[ai][bj][m][0] * sc, v1 = acc[ai][bj][m][1] * sc;
;                     u32x4 w; w.x = cvt_pk_bf16(v0[0], v0[1]); w.y = cvt_pk_bf16(v0[2], v0[3]); w.z = cvt_pk_bf16(v1[0], v1[1]); w.w = cvt_pk_bf16(v1[2], v1[3]);
;                     *(u32x4*)(rowp + bj * HALF) = w;
;                     if (MODE == 0 && t < 2) { float ss = ((v0[0] * v0[0] + v0[1] * v0[1]) + (v0[2] * v0[2] + v0[3] * v0[3])) + ((v1[0] * v1[0] + v1[1] * v1[1]) + (v1[2] * v1[2] + v1[3] * v1[3]));
;                         ss += __shfl_xor(ss, 16); ss += __shfl_xor(ss, 32);
;                         if (fq == 0) nrm[(size_t)(t * 32 + 8 * (pn & 3) + 4 * bj + wc) * nrows + (row0 + ai * HALF + m * 16)] = ss; } } }
.LBB0_280:
	v_add_co_u32_e32 v52, vcc, 0x48000, v148
	v_pk_mul_f32 v[46:47], v[56:57], v[46:47]
	s_nop 0
	v_addc_co_u32_e32 v53, vcc, 0, v149, vcc
	v_pk_mul_f32 v[44:45], v[146:147], v[44:45]
	v_pk_mul_f32 v[42:43], v[56:57], v[42:43]
	v_pk_mul_f32 v[40:41], v[146:147], v[40:41]
	s_and_b64 vcc, exec, s[12:13]
	v_cvt_pk_bf16_f32 v48, v44, v45
	s_waitcnt lgkmcnt(0)
	v_cvt_pk_bf16_f32 v49, v46, v47
	v_cvt_pk_bf16_f32 v50, v40, v41
	v_cvt_pk_bf16_f32 v51, v42, v43
	global_store_dwordx4 v[52:53], v[48:51], off
	s_cbranch_vccnz .LBB0_284
	v_mul_f32_e32 v41, v41, v41
	v_fmac_f32_e32 v41, v40, v40
	v_mul_f32_e32 v40, v43, v43
	v_mul_f32_e32 v45, v45, v45
	v_fmac_f32_e32 v40, v42, v42
	v_and_b32_e32 v42, 64, v157
	v_fmac_f32_e32 v45, v44, v44
	v_mul_f32_e32 v44, v47, v47
	v_add_f32_e32 v40, v41, v40
	v_xor_b32_e32 v41, 16, v157
	v_add_u32_e32 v42, 64, v42
	v_fmac_f32_e32 v44, v46, v46
	v_cmp_lt_i32_e32 vcc, v41, v42
	v_add_f32_e32 v44, v45, v44
	v_add_f32_e32 v40, v44, v40
	v_cndmask_b32_e32 v41, v157, v41, vcc
	v_lshlrev_b32_e32 v41, 2, v41
	v_mov_b32_e32 v41, v40
	s_nop 1
	v_permlane16_swap_b32_e32 v41, v40
	s_waitcnt lgkmcnt(0)
	v_add_f32_e32 v40, v40, v41
	v_xor_b32_e32 v41, 32, v157
	v_cmp_lt_i32_e32 vcc, v41, v42
	s_nop 1
	v_cndmask_b32_e32 v41, v157, v41, vcc
	v_lshlrev_b32_e32 v41, 2, v41
	v_mov_b32_e32 v41, v40
	s_nop 1
	v_permlane32_swap_b32_e32 v41, v40
	s_and_saveexec_b64 s[36:37], s[8:9]
	s_cbranch_execz .LBB0_283
	s_ashr_i32 s31, s30, 31
	s_lshl_b64 s[40:41], s[30:31], 16
	s_add_u32 s40, s50, s40
	s_addc_u32 s41, s51, s41
	s_waitcnt lgkmcnt(0)
	v_add_f32_e32 v42, v40, v41
	v_lshl_add_u64 v[40:41], v[144:145], 2, s[40:41]
	global_store_dword v[40:41], v42, off offset:576

; __device__ __forceinline__ unsigned cvt_pk_bf16(float lo, float hi) { unsigned r; asm volatile("v_cvt_pk_bf16_f32 %0, %1, %2" : "=v"(r) : "v"(lo), "v"(hi)); return r; }
;     __device__ __forceinline__ void operator()(const f32x4 (&acc)[2][2][4][2], const Unit& u, int wr, int wc, int fr, int fq) const {
;     ...
;             for (int m = 0; m < 4; ++m) { bf16_t* rowp = base + (size_t)(row0 + ai * HALF + m * 16) * ldc + col0;
; #pragma unroll
;                 for (int bj = 0; bj < 2; ++bj) { const f32x4 v0 = acc[ai][bj][m][0] * sc, v1 = acc[ai][bj][m][1] * sc;
;                     u32x4 w; w.x = cvt_pk_bf16(v0[0], v0[1]); w.y = cvt_pk_bf16(v0[2], v0[3]); w.z = cvt_pk_bf16(v1[0], v1[1]); w.w = cvt_pk_bf16(v1[2], v1[3]);
;                     *(u32x4*)(rowp + bj * HALF) = w;
;                     if (MODE == 0 && t < 2) { float ss = ((v0[0] * v0[0] + v0[1] * v0[1]) + (v0[2] * v0[2] + v0[3] * v0[3])) + ((v1[0] * v1[0] + v1[1] * v1[1]) + (v1[2] * v1[2] + v1[3] * v1[3]));
;                         ss += __shfl_xor(ss, 16); ss += __shfl_xor(ss, 32);
;                         if (fq == 0) nrm[(size_t)(t * 32 + 8 * (pn & 3) + 4 * bj + wc) * nrows + (row0 + ai * HALF + m * 16)] = ss; } } }
.LBB0_284:
	s_mov_b64 s[36:37], 0x48000
	v_mov_b32_e32 v40, v146
	s_waitcnt lgkmcnt(0)
	v_mov_b32_e32 v41, v146
	v_lshl_add_u64 v[46:47], v[148:149], 0, s[36:37]
	v_pk_mul_f32 v[38:39], v[40:41], v[38:39]
	v_pk_mul_f32 v[36:37], v[146:147], v[36:37]
	v_pk_mul_f32 v[34:35], v[40:41], v[34:35]
	v_pk_mul_f32 v[32:33], v[146:147], v[32:33]
	s_and_b64 vcc, exec, s[12:13]
	v_cvt_pk_bf16_f32 v42, v36, v37
	v_cvt_pk_bf16_f32 v43, v38, v39
	v_cvt_pk_bf16_f32 v44, v32, v33
	v_cvt_pk_bf16_f32 v45, v34, v35
	global_store_dwordx4 v[46:47], v[42:45], off offset:256
	s_cbranch_vccnz .LBB0_288
	v_mul_f32_e32 v33, v33, v33
	v_fmac_f32_e32 v33, v32, v32
	v_mul_f32_e32 v32, v35, v35
	v_mul_f32_e32 v37, v37, v37
	v_fmac_f32_e32 v32, v34, v34
	v_and_b32_e32 v34, 64, v157
	v_fmac_f32_e32 v37, v36, v36
	v_mul_f32_e32 v36, v39, v39
	v_add_f32_e32 v32, v33, v32
	v_xor_b32_e32 v33, 16, v157
	v_add_u32_e32 v34, 64, v34
	v_fmac_f32_e32 v36, v38, v38
	v_cmp_lt_i32_e32 vcc, v33, v34
	v_add_f32_e32 v36, v37, v36
	v_add_f32_e32 v32, v36, v32
	v_cndmask_b32_e32 v33, v157, v33, vcc
	v_lshlrev_b32_e32 v33, 2, v33
	v_mov_b32_e32 v33, v32
	s_nop 1
	v_permlane16_swap_b32_e32 v33, v32
	s_waitcnt lgkmcnt(0)
	v_add_f32_e32 v32, v32, v33
	v_xor_b32_e32 v33, 32, v157
	v_cmp_lt_i32_e32 vcc, v33, v34
	s_nop 1
	v_cndmask_b32_e32 v33, v157, v33, vcc
	v_lshlrev_b32_e32 v33, 2, v33
	v_mov_b32_e32 v33, v32
	s_nop 1
	v_permlane32_swap_b32_e32 v33, v32
	s_and_saveexec_b64 s[36:37], s[8:9]
	s_cbranch_execz .LBB0_287
	s_or_b32 s40, s30, 4
	s_ashr_i32 s41, s40, 31
	s_lshl_b64 s[40:41], s[40:41], 16
	s_add_u32 s40, s50, s40
	s_addc_u32 s41, s51, s41
	s_waitcnt lgkmcnt(0)
	v_add_f32_e32 v34, v32, v33
	v_lshl_add_u64 v[32:33], v[144:145], 2, s[40:41]
	global_store_dword v[32:33], v34, off offset:576

; __device__ __forceinline__ unsigned cvt_pk_bf16(float lo, float hi) { unsigned r; asm volatile("v_cvt_pk_bf16_f32 %0, %1, %2" : "=v"(r) : "v"(lo), "v"(hi)); return r; }
;     __device__ __forceinline__ void operator()(const f32x4 (&acc)[2][2][4][2], const Unit& u, int wr, int wc, int fr, int fq) const {
;     ...
;             for (int m = 0; m < 4; ++m) { bf16_t* rowp = base + (size_t)(row0 + ai * HALF + m * 16) * ldc + col0;
; #pragma unroll
;                 for (int bj = 0; bj < 2; ++bj) { const f32x4 v0 = acc[ai][bj][m][0] * sc, v1 = acc[ai][bj][m][1] * sc;
;                     u32x4 w; w.x = cvt_pk_bf16(v0[0], v0[1]); w.y = cvt_pk_bf16(v0[2], v0[3]); w.z = cvt_pk_bf16(v1[0], v1[1]); w.w = cvt_pk_bf16(v1[2], v1[3]);
;                     *(u32x4*)(rowp + bj * HALF) = w;
;                     if (MODE == 0 && t < 2) { float ss = ((v0[0] * v0[0] + v0[1] * v0[1]) + (v0[2] * v0[2] + v0[3] * v0[3])) + ((v1[0] * v1[0] + v1[1] * v1[1]) + (v1[2] * v1[2] + v1[3] * v1[3]));
;                         ss += __shfl_xor(ss, 16); ss += __shfl_xor(ss, 32);
;                         if (fq == 0) nrm[(size_t)(t * 32 + 8 * (pn & 3) + 4 * bj + wc) * nrows + (row0 + ai * HALF + m * 16)] = ss; } } }
.LBB0_288:
	v_add_co_u32_e32 v36, vcc, 0x50000, v148
	v_pk_mul_f32 v[30:31], v[40:41], v[30:31]
	s_nop 0
	v_addc_co_u32_e32 v37, vcc, 0, v149, vcc
	v_pk_mul_f32 v[28:29], v[146:147], v[28:29]
	v_pk_mul_f32 v[26:27], v[40:41], v[26:27]
	v_pk_mul_f32 v[24:25], v[146:147], v[24:25]
	s_and_b64 vcc, exec, s[12:13]
	v_cvt_pk_bf16_f32 v32, v28, v29
	s_waitcnt lgkmcnt(0)
	v_cvt_pk_bf16_f32 v33, v30, v31
	v_cvt_pk_bf16_f32 v34, v24, v25
	v_cvt_pk_bf16_f32 v35, v26, v27
	global_store_dwordx4 v[36:37], v[32:35], off
	s_cbranch_vccnz .LBB0_292
	v_mul_f32_e32 v25, v25, v25
	v_fmac_f32_e32 v25, v24, v24
	v_mul_f32_e32 v24, v27, v27
	v_mul_f32_e32 v29, v29, v29
	v_fmac_f32_e32 v24, v26, v26
	v_and_b32_e32 v26, 64, v157
	v_fmac_f32_e32 v29, v28, v28
	v_mul_f32_e32 v28, v31, v31
	v_add_f32_e32 v24, v25, v24
	v_xor_b32_e32 v25, 16, v157
	v_add_u32_e32 v26, 64, v26
	v_fmac_f32_e32 v28, v30, v30
	v_cmp_lt_i32_e32 vcc, v25, v26
	v_add_f32_e32 v28, v29, v28
	v_add_f32_e32 v24, v28, v24
	v_cndmask_b32_e32 v25, v157, v25, vcc
	v_lshlrev_b32_e32 v25, 2, v25
	v_mov_b32_e32 v25, v24
	s_nop 1
	v_permlane16_swap_b32_e32 v25, v24
	s_waitcnt lgkmcnt(0)
	v_add_f32_e32 v24, v24, v25
	v_xor_b32_e32 v25, 32, v157
	v_cmp_lt_i32_e32 vcc, v25, v26
	s_nop 1
	v_cndmask_b32_e32 v25, v157, v25, vcc
	v_lshlrev_b32_e32 v25, 2, v25
	v_mov_b32_e32 v25, v24
	s_nop 1
	v_permlane32_swap_b32_e32 v25, v24
	s_and_saveexec_b64 s[36:37], s[8:9]
	s_cbranch_execz .LBB0_291
	s_ashr_i32 s31, s30, 31
	s_lshl_b64 s[40:41], s[30:31], 16
	s_add_u32 s40, s50, s40
	s_addc_u32 s41, s51, s41
	s_waitcnt lgkmcnt(0)
	v_add_f32_e32 v26, v24, v25
	v_lshl_add_u64 v[24:25], v[144:145], 2, s[40:41]
	global_store_dword v[24:25], v26, off offset:640

; __device__ __forceinline__ unsigned cvt_pk_bf16(float lo, float hi) { unsigned r; asm volatile("v_cvt_pk_bf16_f32 %0, %1, %2" : "=v"(r) : "v"(lo), "v"(hi)); return r; }
;     __device__ __forceinline__ void operator()(const f32x4 (&acc)[2][2][4][2], const Unit& u, int wr, int wc, int fr, int fq) const {
;     ...
;             for (int m = 0; m < 4; ++m) { bf16_t* rowp = base + (size_t)(row0 + ai * HALF + m * 16) * ldc + col0;
; #pragma unroll
;                 for (int bj = 0; bj < 2; ++bj) { const f32x4 v0 = acc[ai][bj][m][0] * sc, v1 = acc[ai][bj][m][1] * sc;
;                     u32x4 w; w.x = cvt_pk_bf16(v0[0], v0[1]); w.y = cvt_pk_bf16(v0[2], v0[3]); w.z = cvt_pk_bf16(v1[0], v1[1]); w.w = cvt_pk_bf16(v1[2], v1[3]);
;                     *(u32x4*)(rowp + bj * HALF) = w;
;                     if (MODE == 0 && t < 2) { float ss = ((v0[0] * v0[0] + v0[1] * v0[1]) + (v0[2] * v0[2] + v0[3] * v0[3])) + ((v1[0] * v1[0] + v1[1] * v1[1]) + (v1[2] * v1[2] + v1[3] * v1[3]));
;                         ss += __shfl_xor(ss, 16); ss += __shfl_xor(ss, 32);
;                         if (fq == 0) nrm[(size_t)(t * 32 + 8 * (pn & 3) + 4 * bj + wc) * nrows + (row0 + ai * HALF + m * 16)] = ss; } } }
.LBB0_292:
	s_mov_b64 s[36:37], 0x50000
	v_mov_b32_e32 v24, v146
	s_waitcnt lgkmcnt(0)
	v_mov_b32_e32 v25, v146
	v_lshl_add_u64 v[30:31], v[148:149], 0, s[36:37]
	v_pk_mul_f32 v[22:23], v[24:25], v[22:23]
	v_pk_mul_f32 v[20:21], v[146:147], v[20:21]
	v_pk_mul_f32 v[18:19], v[24:25], v[18:19]
	v_pk_mul_f32 v[16:17], v[146:147], v[16:17]
	s_and_b64 vcc, exec, s[12:13]
	v_cvt_pk_bf16_f32 v26, v20, v21
	v_cvt_pk_bf16_f32 v27, v22, v23
	v_cvt_pk_bf16_f32 v28, v16, v17
	v_cvt_pk_bf16_f32 v29, v18, v19
	global_store_dwordx4 v[30:31], v[26:29], off offset:256
	s_cbranch_vccnz .LBB0_296
	v_mul_f32_e32 v17, v17, v17
	v_fmac_f32_e32 v17, v16, v16
	v_mul_f32_e32 v16, v19, v19
	v_mul_f32_e32 v21, v21, v21
	v_fmac_f32_e32 v16, v18, v18
	v_and_b32_e32 v18, 64, v157
	v_fmac_f32_e32 v21, v20, v20
	v_mul_f32_e32 v20, v23, v23
	v_add_f32_e32 v16, v17, v16
	v_xor_b32_e32 v17, 16, v157
	v_add_u32_e32 v18, 64, v18
	v_fmac_f32_e32 v20, v22, v22
	v_cmp_lt_i32_e32 vcc, v17, v18
	v_add_f32_e32 v20, v21, v20
	v_add_f32_e32 v16, v20, v16
	v_cndmask_b32_e32 v17, v157, v17, vcc
	v_lshlrev_b32_e32 v17, 2, v17
	v_mov_b32_e32 v17, v16
	s_nop 1
	v_permlane16_swap_b32_e32 v17, v16
	s_waitcnt lgkmcnt(0)
	v_add_f32_e32 v16, v16, v17
	v_xor_b32_e32 v17, 32, v157
	v_cmp_lt_i32_e32 vcc, v17, v18
	s_nop 1
	v_cndmask_b32_e32 v17, v157, v17, vcc
	v_lshlrev_b32_e32 v17, 2, v17
	v_mov_b32_e32 v17, v16
	s_nop 1
	v_permlane32_swap_b32_e32 v17, v16
	s_and_saveexec_b64 s[36:37], s[8:9]
	s_cbranch_execz .LBB0_295
	s_or_b32 s40, s30, 4
	s_ashr_i32 s41, s40, 31
	s_lshl_b64 s[40:41], s[40:41], 16
	s_add_u32 s40, s50, s40
	s_addc_u32 s41, s51, s41
	s_waitcnt lgkmcnt(0)
	v_add_f32_e32 v18, v16, v17
	v_lshl_add_u64 v[16:17], v[144:145], 2, s[40:41]
	global_store_dword v[16:17], v18, off offset:640

; __device__ __forceinline__ unsigned cvt_pk_bf16(float lo, float hi) { unsigned r; asm volatile("v_cvt_pk_bf16_f32 %0, %1, %2" : "=v"(r) : "v"(lo), "v"(hi)); return r; }
;     __device__ __forceinline__ void operator()(const f32x4 (&acc)[2][2][4][2], const Unit& u, int wr, int wc, int fr, int fq) const {
;     ...
;             for (int m = 0; m < 4; ++m) { bf16_t* rowp = base + (size_t)(row0 + ai * HALF + m * 16) * ldc + col0;
; #pragma unroll
;                 for (int bj = 0; bj < 2; ++bj) { const f32x4 v0 = acc[ai][bj][m][0] * sc, v1 = acc[ai][bj][m][1] * sc;
;                     u32x4 w; w.x = cvt_pk_bf16(v0[0], v0[1]); w.y = cvt_pk_bf16(v0[2], v0[3]); w.z = cvt_pk_bf16(v1[0], v1[1]); w.w = cvt_pk_bf16(v1[2], v1[3]);
;                     *(u32x4*)(rowp + bj * HALF) = w;
;                     if (MODE == 0 && t < 2) { float ss = ((v0[0] * v0[0] + v0[1] * v0[1]) + (v0[2] * v0[2] + v0[3] * v0[3])) + ((v1[0] * v1[0] + v1[1] * v1[1]) + (v1[2] * v1[2] + v1[3] * v1[3]));
;                         ss += __shfl_xor(ss, 16); ss += __shfl_xor(ss, 32);
;                         if (fq == 0) nrm[(size_t)(t * 32 + 8 * (pn & 3) + 4 * bj + wc) * nrows + (row0 + ai * HALF + m * 16)] = ss; } } }
.LBB0_296:
	v_add_co_u32_e32 v20, vcc, 0x58000, v148
	v_pk_mul_f32 v[14:15], v[24:25], v[14:15]
	s_nop 0
	v_addc_co_u32_e32 v21, vcc, 0, v149, vcc
	v_pk_mul_f32 v[12:13], v[146:147], v[12:13]
	v_pk_mul_f32 v[10:11], v[24:25], v[10:11]
	v_pk_mul_f32 v[8:9], v[146:147], v[8:9]
	s_and_b64 vcc, exec, s[12:13]
	v_cvt_pk_bf16_f32 v16, v12, v13
	s_waitcnt lgkmcnt(0)
	v_cvt_pk_bf16_f32 v17, v14, v15
	v_cvt_pk_bf16_f32 v18, v8, v9
	v_cvt_pk_bf16_f32 v19, v10, v11
	global_store_dwordx4 v[20:21], v[16:19], off
	s_cbranch_vccnz .LBB0_300
	v_mul_f32_e32 v9, v9, v9
	v_fmac_f32_e32 v9, v8, v8
	v_mul_f32_e32 v8, v11, v11
	v_mul_f32_e32 v13, v13, v13
	v_fmac_f32_e32 v8, v10, v10
	v_and_b32_e32 v10, 64, v157
	v_fmac_f32_e32 v13, v12, v12
	v_mul_f32_e32 v12, v15, v15
	v_add_f32_e32 v8, v9, v8
	v_xor_b32_e32 v9, 16, v157
	v_add_u32_e32 v10, 64, v10
	v_fmac_f32_e32 v12, v14, v14
	v_cmp_lt_i32_e32 vcc, v9, v10
	v_add_f32_e32 v12, v13, v12
	v_add_f32_e32 v8, v12, v8
	v_cndmask_b32_e32 v9, v157, v9, vcc
	v_lshlrev_b32_e32 v9, 2, v9
	v_mov_b32_e32 v9, v8
	s_nop 1
	v_permlane16_swap_b32_e32 v9, v8
	s_waitcnt lgkmcnt(0)
	v_add_f32_e32 v8, v8, v9
	v_xor_b32_e32 v9, 32, v157
	v_cmp_lt_i32_e32 vcc, v9, v10
	s_nop 1
	v_cndmask_b32_e32 v9, v157, v9, vcc
	v_lshlrev_b32_e32 v9, 2, v9
	v_mov_b32_e32 v9, v8
	s_nop 1
	v_permlane32_swap_b32_e32 v9, v8
	s_and_saveexec_b64 s[36:37], s[8:9]
	s_cbranch_execz .LBB0_299
	s_ashr_i32 s31, s30, 31
	s_lshl_b64 s[40:41], s[30:31], 16
	s_add_u32 s40, s50, s40
	s_addc_u32 s41, s51, s41
	s_waitcnt lgkmcnt(0)
	v_add_f32_e32 v10, v8, v9
	v_lshl_add_u64 v[8:9], v[144:145], 2, s[40:41]
	global_store_dword v[8:9], v10, off offset:704

; __device__ __forceinline__ unsigned cvt_pk_bf16(float lo, float hi) { unsigned r; asm volatile("v_cvt_pk_bf16_f32 %0, %1, %2" : "=v"(r) : "v"(lo), "v"(hi)); return r; }
;     __device__ __forceinline__ void operator()(const f32x4 (&acc)[2][2][4][2], const Unit& u, int wr, int wc, int fr, int fq) const {
;     ...
;             for (int m = 0; m < 4; ++m) { bf16_t* rowp = base + (size_t)(row0 + ai * HALF + m * 16) * ldc + col0;
; #pragma unroll
;                 for (int bj = 0; bj < 2; ++bj) { const f32x4 v0 = acc[ai][bj][m][0] * sc, v1 = acc[ai][bj][m][1] * sc;
;                     u32x4 w; w.x = cvt_pk_bf16(v0[0], v0[1]); w.y = cvt_pk_bf16(v0[2], v0[3]); w.z = cvt_pk_bf16(v1[0], v1[1]); w.w = cvt_pk_bf16(v1[2], v1[3]);
;                     *(u32x4*)(rowp + bj * HALF) = w;
;                     if (MODE == 0 && t < 2) { float ss = ((v0[0] * v0[0] + v0[1] * v0[1]) + (v0[2] * v0[2] + v0[3] * v0[3])) + ((v1[0] * v1[0] + v1[1] * v1[1]) + (v1[2] * v1[2] + v1[3] * v1[3]));
;                         ss += __shfl_xor(ss, 16); ss += __shfl_xor(ss, 32);
;                         if (fq == 0) nrm[(size_t)(t * 32 + 8 * (pn & 3) + 4 * bj + wc) * nrows + (row0 + ai * HALF + m * 16)] = ss; } } }
.LBB0_300:
	s_mov_b64 s[36:37], 0x58000
	v_mov_b32_e32 v8, v146
	s_waitcnt lgkmcnt(0)
	v_mov_b32_e32 v9, v146
	v_lshl_add_u64 v[12:13], v[148:149], 0, s[36:37]
	v_pk_mul_f32 v[6:7], v[8:9], v[6:7]
	v_pk_mul_f32 v[4:5], v[146:147], v[4:5]
	v_pk_mul_f32 v[2:3], v[8:9], v[2:3]
	v_pk_mul_f32 v[0:1], v[146:147], v[0:1]
	s_and_b64 vcc, exec, s[12:13]
	v_cvt_pk_bf16_f32 v8, v4, v5
	v_cvt_pk_bf16_f32 v9, v6, v7
	v_cvt_pk_bf16_f32 v10, v0, v1
	v_cvt_pk_bf16_f32 v11, v2, v3
	global_store_dwordx4 v[12:13], v[8:11], off offset:256
	s_cbranch_vccnz .LBB0_304
	v_mul_f32_e32 v1, v1, v1
	v_fmac_f32_e32 v1, v0, v0
	v_mul_f32_e32 v0, v3, v3
	v_mul_f32_e32 v5, v5, v5
	v_fmac_f32_e32 v0, v2, v2
	v_and_b32_e32 v2, 64, v157
	v_fmac_f32_e32 v5, v4, v4
	v_mul_f32_e32 v4, v7, v7
	v_add_f32_e32 v0, v1, v0
	v_xor_b32_e32 v1, 16, v157
	v_add_u32_e32 v2, 64, v2
	v_fmac_f32_e32 v4, v6, v6
	v_cmp_lt_i32_e32 vcc, v1, v2
	v_add_f32_e32 v4, v5, v4
	v_add_f32_e32 v0, v4, v0
	v_cndmask_b32_e32 v1, v157, v1, vcc
	v_lshlrev_b32_e32 v1, 2, v1
	v_mov_b32_e32 v1, v0
	s_nop 1
	v_permlane16_swap_b32_e32 v1, v0
	s_waitcnt lgkmcnt(0)
	v_add_f32_e32 v0, v0, v1
	v_xor_b32_e32 v1, 32, v157
	v_cmp_lt_i32_e32 vcc, v1, v2
	s_nop 1
	v_cndmask_b32_e32 v1, v157, v1, vcc
	v_lshlrev_b32_e32 v1, 2, v1
	v_mov_b32_e32 v1, v0
	s_nop 1
	v_permlane32_swap_b32_e32 v1, v0
	s_and_saveexec_b64 s[12:13], s[8:9]
	s_cbranch_execz .LBB0_303
	s_or_b32 s30, s30, 4
	s_ashr_i32 s31, s30, 31
	s_lshl_b64 s[30:31], s[30:31], 16
	s_add_u32 s30, s50, s30
	s_addc_u32 s31, s51, s31
	s_waitcnt lgkmcnt(0)
	v_add_f32_e32 v2, v0, v1
	v_lshl_add_u64 v[0:1], v[144:145], 2, s[30:31]
	global_store_dword v[0:1], v2, off offset:704

; __device__ __forceinline__ u32x4 pk8(const f32x4 a, const f32x4 b) { u32x4 q; q.x = cvt_pk_bf16(a[0], a[1]); q.y = cvt_pk_bf16(a[2], a[3]); q.z = cvt_pk_bf16(b[0], b[1]); q.w = cvt_pk_bf16(b[2], b[3]); return q; }
;     __device__ __forceinline__ void fused(f32x4 (&acc)[2][2][4][2], const Unit& u, int wr, int wc, int fr, int fq, PG8_LAS unsigned char* lds, int wid, int lane) const {
;     ...
;         const int row0 = u.orow + wr * 64 + fr, col0 = u.ocol * BM + wc * 32 + 8 * fq; const size_t boff = (size_t)(u.orow / rows_per_batch) * gld + col0;
;         { f32x4 gv[2][2];
; #pragma unroll
;           for (int bj = 0; bj < 2; ++bj)
; #pragma unroll
;               for (int n = 0; n < 2; ++n) gv[bj][n] = *(const f32x4*)(gate + boff + bj * HALF + n * 4) * asc;
;           bf16_t* op = out + (size_t)row0 * ldc + col0;
;           if constexpr (XF32) {
;               const float* xp = (const float*)xin + (size_t)row0 * ldc + col0; f32x4 xv[4][2][2];
; #pragma unroll
;               for (int ai = 0; ai < 2; ++ai) {
; #pragma unroll
;                   for (int m = 0; m < 4; ++m)
; #pragma unroll
;                       for (int bj = 0; bj < 2; ++bj)
; #pragma unroll
;                           for (int n = 0; n < 2; ++n) xv[m][bj][n] = *(const f32x4*)(xp + (size_t)(ai * HALF + m * 16) * ldc + bj * HALF + n * 4);
; #pragma unroll
;                   for (int m = 0; m < 4; ++m)
; #pragma unroll
;                       for (int bj = 0; bj < 2; ++bj) { acc[ai][bj][m][0] = xv[m][bj][0] + gv[bj][0] * acc[ai][bj][m][0]; acc[ai][bj][m][1] = xv[m][bj][1] + gv[bj][1] * acc[ai][bj][m][1];
;                           *(u32x4*)(op + (size_t)(ai * HALF + m * 16) * ldc + bj * HALF) = pk8(acc[ai][bj][m][0], acc[ai][bj][m][1]); }
.LBB0_666:
	s_lshl_b32 s6, s36, 5
	v_ashrrev_i32_e32 v128, 1, v187
	s_lshl_b32 s7, s4, 8
	v_and_b32_e32 v128, -8, v128
	s_or_b32 s6, s7, s6
	s_ashr_i32 s8, s3, 31
	v_add_u32_e32 v144, s6, v128
	s_lshr_b32 s6, s8, 20
	s_add_i32 s6, s3, s6
	s_ashr_i32 s6, s6, 12
	v_ashrrev_i32_e32 v145, 31, v144
	v_mov_b32_e32 v128, 0x1800
	v_mad_i64_i32 v[128:129], s[6:7], s6, v128, v[144:145]
	v_lshl_add_u64 v[172:173], v[128:129], 2, s[78:79]
	s_mov_b32 s9, 0x102000
	v_add_co_u32_e32 v128, vcc, s9, v172
	v_add_u32_e32 v146, s3, v186
	v_readlane_b32 s44, v254, 36
	v_addc_co_u32_e32 v129, vcc, 0, v173, vcc
	v_ashrrev_i32_e32 v147, 31, v146
	v_readlane_b32 s45, v254, 37
	v_readlane_b32 s48, v254, 40
	v_readlane_b32 s49, v254, 41
	s_barrier
	global_load_dwordx4 v[132:135], v[128:129], off
	v_lshlrev_b64 v[128:129], 12, v[146:147]
	s_mov_b64 s[48:49], s[44:45]
	s_mov_b64 s[6:7], 0x102000
	v_lshl_add_u64 v[128:129], s[48:49], 0, v[128:129]
	v_lshl_add_u64 v[184:185], v[144:145], 2, v[128:129]
	v_lshl_add_u64 v[128:129], v[172:173], 0, s[6:7]
	s_mov_b32 s6, 0x10000
	s_mov_b64 s[10:11], 0x10000
	v_add_co_u32_e32 v164, vcc, s6, v184
	v_lshl_add_u64 v[166:167], v[184:185], 0, s[10:11]
	s_nop 0
	v_addc_co_u32_e32 v165, vcc, 0, v185, vcc
	s_mov_b64 s[10:11], 0x10200
	s_mov_b32 s7, 0x20000
	global_load_dwordx4 v[148:151], v[184:185], off offset:16
	global_load_dwordx4 v[152:155], v[184:185], off
	global_load_dwordx4 v[140:143], v[128:129], off offset:16
	global_load_dwordx4 v[136:139], v[128:129], off offset:512
	global_load_dwordx4 v[156:159], v[184:185], off offset:528
	global_load_dwordx4 v[160:163], v[184:185], off offset:512
	s_nop 0
	global_load_dwordx4 v[128:131], v[128:129], off offset:528
	s_mov_b32 s9, 0x80000
	global_load_dwordx4 v[190:193], v[164:165], off
	global_load_dwordx4 v[194:197], v[166:167], off offset:16
	v_lshl_add_u64 v[166:167], v[184:185], 0, s[10:11]
	global_load_dwordx4 v[198:201], v[164:165], off offset:512
	global_load_dwordx4 v[202:205], v[166:167], off offset:16
	s_mov_b64 s[10:11], 0x20000
	v_add_co_u32_e32 v164, vcc, s7, v184
	v_lshl_add_u64 v[166:167], v[184:185], 0, s[10:11]
	s_nop 0
	v_addc_co_u32_e32 v165, vcc, 0, v185, vcc
	s_mov_b64 s[10:11], 0x20200
	global_load_dwordx4 v[206:209], v[164:165], off
	global_load_dwordx4 v[210:213], v[166:167], off offset:16
	v_lshl_add_u64 v[166:167], v[184:185], 0, s[10:11]
	s_mov_b64 s[10:11], 0x30000
	s_mov_b32 s7, 0x30000
	global_load_dwordx4 v[214:217], v[164:165], off offset:512
	global_load_dwordx4 v[218:221], v[166:167], off offset:16
	v_add_co_u32_e32 v164, vcc, s7, v184
	v_lshl_add_u64 v[166:167], v[184:185], 0, s[10:11]
	s_nop 0
	v_addc_co_u32_e32 v165, vcc, 0, v185, vcc
	global_load_dwordx4 v[226:229], v[166:167], off offset:16
	s_mov_b64 s[10:11], 0x30200
	global_load_dwordx4 v[222:225], v[164:165], off
	global_load_dwordx4 v[230:233], v[164:165], off offset:512
	v_lshl_add_u64 v[164:165], v[184:185], 0, s[10:11]
	global_load_dwordx4 v[234:237], v[164:165], off offset:16
	v_lshlrev_b64 v[166:167], 11, v[146:147]
	v_lshl_add_u64 v[166:167], s[18:19], 0, v[166:167]
	v_lshl_add_u64 v[182:183], v[144:145], 1, v[166:167]
	s_mov_b32 s7, 0x8000
	s_mov_b32 s10, 0xb0000
	s_lshl_b32 s5, s5, 10
	v_readlane_b32 s56, v254, 48
	v_readlane_b32 s57, v254, 49
	v_readlane_b32 s58, v254, 50
	v_readlane_b32 s59, v254, 51
	v_readlane_b32 s52, v254, 44
	v_readlane_b32 s53, v254, 45
	v_readlane_b32 s54, v254, 46
	v_readlane_b32 s55, v254, 47
	s_mov_b64 s[62:63], s[58:59]
	s_mov_b64 s[60:61], s[56:57]
	s_mov_b64 s[58:59], s[54:55]
	v_readlane_b32 s46, v254, 38
	v_readlane_b32 s47, v254, 39
	v_readlane_b32 s50, v254, 42
	v_readlane_b32 s51, v254, 43
	s_mov_b64 s[56:57], s[52:53]
	s_waitcnt vmcnt(0)
	v_pk_fma_f32 v[180:181], v[120:121], v[140:141], v[148:149]
	v_pk_fma_f32 v[174:175], v[126:127], v[134:135], v[154:155]
	v_pk_fma_f32 v[170:171], v[104:105], v[128:129], v[156:157]
	v_pk_fma_f32 v[176:177], v[124:125], v[132:133], v[152:153]
	v_pk_fma_f32 v[178:179], v[122:123], v[142:143], v[150:151]
	v_pk_fma_f32 v[156:157], v[108:109], v[140:141], v[194:195]
	v_add_co_u32_e32 v108, vcc, s7, v182
	v_cvt_pk_bf16_f32 v120, v176, v177
	v_cvt_pk_bf16_f32 v121, v174, v175
	v_cvt_pk_bf16_f32 v122, v180, v181
	v_cvt_pk_bf16_f32 v123, v178, v179
	s_nop 1
	v_addc_co_u32_e32 v109, vcc, 0, v183, vcc
	global_store_dwordx4 v[182:183], v[120:123], off
	v_pk_fma_f32 v[164:165], v[118:119], v[138:139], v[162:163]
	v_pk_fma_f32 v[166:167], v[116:117], v[136:137], v[160:161]
	v_pk_fma_f32 v[168:169], v[106:107], v[130:131], v[158:159]
	v_cvt_pk_bf16_f32 v104, v166, v167
	v_cvt_pk_bf16_f32 v105, v164, v165
	v_cvt_pk_bf16_f32 v106, v170, v171
	v_pk_fma_f32 v[120:121], v[92:93], v[140:141], v[210:211]
	v_cvt_pk_bf16_f32 v107, v168, v169
	v_add_co_u32_e32 v92, vcc, s6, v182
	global_store_dwordx4 v[182:183], v[104:107], off offset:256
	v_pk_fma_f32 v[160:161], v[114:115], v[134:135], v[192:193]
	v_pk_fma_f32 v[162:163], v[112:113], v[132:133], v[190:191]
	v_pk_fma_f32 v[158:159], v[110:111], v[142:143], v[196:197]
	v_cvt_pk_bf16_f32 v104, v162, v163
	v_cvt_pk_bf16_f32 v105, v160, v161
	v_cvt_pk_bf16_f32 v106, v156, v157
	v_pk_fma_f32 v[150:151], v[98:99], v[138:139], v[200:201]
	v_cvt_pk_bf16_f32 v107, v158, v159
	global_store_dwordx4 v[108:109], v[104:107], off
	v_pk_fma_f32 v[154:155], v[96:97], v[136:137], v[198:199]
	v_pk_fma_f32 v[148:149], v[90:91], v[130:131], v[204:205]
	v_pk_fma_f32 v[152:153], v[88:89], v[128:129], v[202:203]
	v_cvt_pk_bf16_f32 v88, v154, v155
	v_cvt_pk_bf16_f32 v89, v150, v151
	v_addc_co_u32_e32 v93, vcc, 0, v183, vcc
	v_cvt_pk_bf16_f32 v90, v152, v153
	v_cvt_pk_bf16_f32 v91, v148, v149
	s_mov_b32 s6, 0x18000
; __device__ __forceinline__ u32x4 pk8(const f32x4 a, const f32x4 b) { u32x4 q; q.x = cvt_pk_bf16(a[0], a[1]); q.y = cvt_pk_bf16(a[2], a[3]); q.z = cvt_pk_bf16(b[0], b[1]); q.w = cvt_pk_bf16(b[2], b[3]); return q; }
;     __device__ __forceinline__ void fused(f32x4 (&acc)[2][2][4][2], const Unit& u, int wr, int wc, int fr, int fq, PG8_LAS unsigned char* lds, int wid, int lane) const {
;     ...
;               const float* xp = (const float*)xin + (size_t)row0 * ldc + col0; f32x4 xv[4][2][2];
; #pragma unroll
;               for (int ai = 0; ai < 2; ++ai) {
; #pragma unroll
;                   for (int m = 0; m < 4; ++m)
; #pragma unroll
;                       for (int bj = 0; bj < 2; ++bj)
; #pragma unroll
;                           for (int n = 0; n < 2; ++n) xv[m][bj][n] = *(const f32x4*)(xp + (size_t)(ai * HALF + m * 16) * ldc + bj * HALF + n * 4);
; #pragma unroll
;                   for (int m = 0; m < 4; ++m)
; #pragma unroll
;                       for (int bj = 0; bj < 2; ++bj) { acc[ai][bj][m][0] = xv[m][bj][0] + gv[bj][0] * acc[ai][bj][m][0]; acc[ai][bj][m][1] = xv[m][bj][1] + gv[bj][1] * acc[ai][bj][m][1];
;                           *(u32x4*)(op + (size_t)(ai * HALF + m * 16) * ldc + bj * HALF) = pk8(acc[ai][bj][m][0], acc[ai][bj][m][1]); }
	global_store_dwordx4 v[108:109], v[88:91], off offset:256
	v_pk_fma_f32 v[124:125], v[102:103], v[134:135], v[208:209]
	v_pk_fma_f32 v[126:127], v[100:101], v[132:133], v[206:207]
	v_pk_fma_f32 v[122:123], v[94:95], v[142:143], v[212:213]
	v_cvt_pk_bf16_f32 v88, v126, v127
	v_cvt_pk_bf16_f32 v89, v124, v125
	v_cvt_pk_bf16_f32 v90, v120, v121
	v_pk_fma_f32 v[118:119], v[80:81], v[136:137], v[214:215]
	v_cvt_pk_bf16_f32 v91, v122, v123
	global_store_dwordx4 v[92:93], v[88:91], off
	v_pk_fma_f32 v[116:117], v[72:73], v[128:129], v[218:219]
	v_cvt_pk_bf16_f32 v72, v118, v119
	v_pk_fma_f32 v[104:105], v[76:77], v[140:141], v[226:227]
	v_add_co_u32_e32 v76, vcc, s6, v182
	v_pk_fma_f32 v[114:115], v[82:83], v[138:139], v[216:217]
	v_pk_fma_f32 v[112:113], v[74:75], v[130:131], v[220:221]
	v_cvt_pk_bf16_f32 v73, v114, v115
	v_cvt_pk_bf16_f32 v74, v116, v117
	v_pk_fma_f32 v[110:111], v[84:85], v[132:133], v[222:223]
	v_cvt_pk_bf16_f32 v75, v112, v113
	global_store_dwordx4 v[92:93], v[72:75], off offset:256
	v_addc_co_u32_e32 v77, vcc, 0, v183, vcc
	s_nop 0
	v_cvt_pk_bf16_f32 v72, v110, v111
	v_pk_fma_f32 v[108:109], v[86:87], v[134:135], v[224:225]
	v_pk_fma_f32 v[106:107], v[78:79], v[142:143], v[228:229]
	v_cvt_pk_bf16_f32 v73, v108, v109
	v_cvt_pk_bf16_f32 v74, v104, v105
	v_pk_fma_f32 v[90:91], v[70:71], v[138:139], v[232:233]
	v_cvt_pk_bf16_f32 v75, v106, v107
	global_store_dwordx4 v[76:77], v[72:75], off
	v_pk_fma_f32 v[94:95], v[68:69], v[136:137], v[230:231]
	v_pk_fma_f32 v[88:89], v[66:67], v[130:131], v[236:237]
	v_pk_fma_f32 v[92:93], v[64:65], v[128:129], v[234:235]
	v_cvt_pk_bf16_f32 v64, v94, v95
	v_cvt_pk_bf16_f32 v65, v90, v91
	s_mov_b64 s[6:7], 0x80000
	v_cvt_pk_bf16_f32 v66, v92, v93
	v_cvt_pk_bf16_f32 v67, v88, v89
	global_store_dwordx4 v[76:77], v[64:67], off offset:256
	v_add_co_u32_e32 v72, vcc, s9, v184
	v_lshl_add_u64 v[68:69], v[184:185], 0, s[6:7]
	s_nop 0
	v_addc_co_u32_e32 v73, vcc, 0, v185, vcc
	s_mov_b64 s[6:7], 0x80200
	s_mov_b32 s9, 0x90000
	global_load_dwordx4 v[64:67], v[72:73], off
	v_lshl_add_u64 v[76:77], v[184:185], 0, s[6:7]
	s_mov_b64 s[6:7], 0x90000
	v_add_co_u32_e32 v80, vcc, s9, v184
	v_lshl_add_u64 v[82:83], v[184:185], 0, s[6:7]
	s_nop 0
	v_addc_co_u32_e32 v81, vcc, 0, v185, vcc
	s_mov_b64 s[6:7], 0x90200
	s_mov_b32 s9, 0xa0000
	global_load_dwordx4 v[68:71], v[68:69], off offset:16
	s_nop 0
	global_load_dwordx4 v[72:75], v[72:73], off offset:512
	s_nop 0
	global_load_dwordx4 v[76:79], v[76:77], off offset:16
	s_waitcnt vmcnt(3)
	v_pk_fma_f32 v[102:103], v[60:61], v[132:133], v[64:65]
	global_load_dwordx4 v[190:193], v[80:81], off
	global_load_dwordx4 v[194:197], v[82:83], off offset:16
	v_lshl_add_u64 v[82:83], v[184:185], 0, s[6:7]
	global_load_dwordx4 v[198:201], v[80:81], off offset:512
	global_load_dwordx4 v[202:205], v[82:83], off offset:16
	s_mov_b64 s[6:7], 0xa0000
	v_add_co_u32_e32 v80, vcc, s9, v184
	v_lshl_add_u64 v[82:83], v[184:185], 0, s[6:7]
	s_nop 0
	v_addc_co_u32_e32 v81, vcc, 0, v185, vcc
	s_mov_b64 s[6:7], 0xa0200
	global_load_dwordx4 v[206:209], v[80:81], off
	global_load_dwordx4 v[210:213], v[82:83], off offset:16
	v_lshl_add_u64 v[82:83], v[184:185], 0, s[6:7]
	global_load_dwordx4 v[214:217], v[80:81], off offset:512
	global_load_dwordx4 v[218:221], v[82:83], off offset:16
	s_mov_b64 s[6:7], 0xb0000
	v_add_co_u32_e32 v80, vcc, s10, v184
	s_lshl_b32 s9, s36, 2
	s_nop 0
	v_addc_co_u32_e32 v81, vcc, 0, v185, vcc
	v_lshl_add_u64 v[82:83], v[184:185], 0, s[6:7]
	global_load_dwordx4 v[222:225], v[80:81], off
	global_load_dwordx4 v[226:229], v[82:83], off offset:16
	s_add_i32 s6, s9, 0
	s_add_i32 s5, s6, s5
	s_mov_b64 s[6:7], 0xb0200
	v_lshl_add_u64 v[82:83], v[184:185], 0, s[6:7]
	global_load_dwordx4 v[230:233], v[80:81], off offset:512
	global_load_dwordx4 v[234:237], v[82:83], off offset:16
	s_mov_b32 s6, 0x40000
	v_add_co_u32_e32 v60, vcc, s6, v182
	s_mov_b32 s6, 0x48000
	s_nop 0
	v_addc_co_u32_e32 v61, vcc, 0, v183, vcc
	s_waitcnt vmcnt(13)
	v_pk_fma_f32 v[86:87], v[48:49], v[136:137], v[72:73]
	v_pk_fma_f32 v[100:101], v[62:63], v[134:135], v[66:67]
	v_pk_fma_f32 v[96:97], v[56:57], v[140:141], v[68:69]
	v_cvt_pk_bf16_f32 v56, v102, v103
	v_cvt_pk_bf16_f32 v57, v100, v101
	v_pk_fma_f32 v[98:99], v[58:59], v[142:143], v[70:71]
	v_cvt_pk_bf16_f32 v58, v96, v97
	v_pk_fma_f32 v[82:83], v[50:51], v[138:139], v[74:75]
	v_cvt_pk_bf16_f32 v59, v98, v99
	global_store_dwordx4 v[60:61], v[56:59], off
	s_waitcnt vmcnt(13)
	v_pk_fma_f32 v[84:85], v[40:41], v[128:129], v[76:77]
	v_cvt_pk_bf16_f32 v40, v86, v87
	v_cvt_pk_bf16_f32 v41, v82, v83
	v_pk_fma_f32 v[80:81], v[42:43], v[130:131], v[78:79]
	v_cvt_pk_bf16_f32 v42, v84, v85
	s_waitcnt vmcnt(12)
	v_pk_fma_f32 v[76:77], v[54:55], v[134:135], v[192:193]
	s_waitcnt vmcnt(11)
	v_pk_fma_f32 v[72:73], v[44:45], v[140:141], v[194:195]
	v_add_co_u32_e32 v44, vcc, s6, v182
	s_mov_b32 s6, 0x50000
	s_nop 0
	v_addc_co_u32_e32 v45, vcc, 0, v183, vcc
	v_cvt_pk_bf16_f32 v43, v80, v81
	global_store_dwordx4 v[60:61], v[40:43], off offset:256
	v_pk_fma_f32 v[78:79], v[52:53], v[132:133], v[190:191]
	v_pk_fma_f32 v[74:75], v[46:47], v[142:143], v[196:197]
	v_cvt_pk_bf16_f32 v40, v78, v79
	s_waitcnt vmcnt(8)
	v_pk_fma_f32 v[56:57], v[28:29], v[140:141], v[210:211]
	v_add_co_u32_e32 v28, vcc, s6, v182
	v_cvt_pk_bf16_f32 v41, v76, v77
	s_mov_b32 s6, 0x58000
	s_nop 0
	v_addc_co_u32_e32 v29, vcc, 0, v183, vcc
	v_cvt_pk_bf16_f32 v42, v72, v73
	v_cvt_pk_bf16_f32 v43, v74, v75
	global_store_dwordx4 v[44:45], v[40:43], off
	v_pk_fma_f32 v[66:67], v[34:35], v[138:139], v[200:201]
	v_pk_fma_f32 v[70:71], v[32:33], v[136:137], v[198:199]
	v_pk_fma_f32 v[64:65], v[26:27], v[130:131], v[204:205]
	v_pk_fma_f32 v[68:69], v[24:25], v[128:129], v[202:203]
	v_cvt_pk_bf16_f32 v24, v70, v71
	v_cvt_pk_bf16_f32 v25, v66, v67
	s_waitcnt vmcnt(5)
; __device__ __forceinline__ u32x4 pk8(const f32x4 a, const f32x4 b) { u32x4 q; q.x = cvt_pk_bf16(a[0], a[1]); q.y = cvt_pk_bf16(a[2], a[3]); q.z = cvt_pk_bf16(b[0], b[1]); q.w = cvt_pk_bf16(b[2], b[3]); return q; }
;     __device__ __forceinline__ bool run(const f32x4 (&v)[2][2][4][2], const Unit& u, int wr, int wc, int fr, int fq, PG8_LAS unsigned char* lds, int wid, int lane) const {
;     ...
;             for (int m = 0; m < 4; ++m) { float s = 0.f;
; #pragma unroll
;                 for (int bj = 0; bj < 2; ++bj)
; #pragma unroll
;                     for (int n = 0; n < 2; ++n) { const f32x4 x = v[ai][bj][m][n]; s += (x[0] * x[0] + x[1] * x[1]) + (x[2] * x[2] + x[3] * x[3]); }
;                 s += __shfl_xor(s, 16); s += __shfl_xor(s, 32);
;                 if (fq == 0) P[(ai * HALF + wr * 64 + m * 16 + fr) * 4 + wc] = s; }
;     __device__ __forceinline__ void fused(f32x4 (&acc)[2][2][4][2], const Unit& u, int wr, int wc, int fr, int fq, PG8_LAS unsigned char* lds, int wid, int lane) const {
;     ...
;                           for (int n = 0; n < 2; ++n) xv[m][bj][n] = *(const f32x4*)(xp + (size_t)(ai * HALF + m * 16) * ldc + bj * HALF + n * 4);
; #pragma unroll
;                   for (int m = 0; m < 4; ++m)
; #pragma unroll
;                       for (int bj = 0; bj < 2; ++bj) { acc[ai][bj][m][0] = xv[m][bj][0] + gv[bj][0] * acc[ai][bj][m][0]; acc[ai][bj][m][1] = xv[m][bj][1] + gv[bj][1] * acc[ai][bj][m][1];
;                           *(u32x4*)(op + (size_t)(ai * HALF + m * 16) * ldc + bj * HALF) = pk8(acc[ai][bj][m][0], acc[ai][bj][m][1]); }
	v_pk_fma_f32 v[40:41], v[12:13], v[140:141], v[226:227]
	v_cvt_pk_bf16_f32 v26, v68, v69
	v_cvt_pk_bf16_f32 v27, v64, v65
	v_add_co_u32_e32 v12, vcc, s6, v182
	global_store_dwordx4 v[44:45], v[24:27], off offset:256
	v_pk_fma_f32 v[60:61], v[38:39], v[134:135], v[208:209]
	v_pk_fma_f32 v[62:63], v[36:37], v[132:133], v[206:207]
	v_pk_fma_f32 v[58:59], v[30:31], v[142:143], v[212:213]
	v_cvt_pk_bf16_f32 v24, v62, v63
	v_cvt_pk_bf16_f32 v25, v60, v61
	v_cvt_pk_bf16_f32 v26, v56, v57
	v_pk_fma_f32 v[50:51], v[18:19], v[138:139], v[216:217]
	v_cvt_pk_bf16_f32 v27, v58, v59
	global_store_dwordx4 v[28:29], v[24:27], off
	v_pk_fma_f32 v[54:55], v[16:17], v[136:137], v[214:215]
	v_pk_fma_f32 v[48:49], v[10:11], v[130:131], v[220:221]
	v_pk_fma_f32 v[52:53], v[8:9], v[128:129], v[218:219]
	v_cvt_pk_bf16_f32 v8, v54, v55
	v_cvt_pk_bf16_f32 v9, v50, v51
	v_addc_co_u32_e32 v13, vcc, 0, v183, vcc
	v_cvt_pk_bf16_f32 v10, v52, v53
	v_cvt_pk_bf16_f32 v11, v48, v49
	global_store_dwordx4 v[28:29], v[8:11], off offset:256
	v_pk_fma_f32 v[44:45], v[22:23], v[134:135], v[224:225]
	v_pk_fma_f32 v[46:47], v[20:21], v[132:133], v[222:223]
	v_pk_fma_f32 v[42:43], v[14:15], v[142:143], v[228:229]
	v_cvt_pk_bf16_f32 v8, v46, v47
	v_cvt_pk_bf16_f32 v9, v44, v45
	v_cvt_pk_bf16_f32 v10, v40, v41
	s_waitcnt vmcnt(7)
	v_pk_fma_f32 v[34:35], v[6:7], v[138:139], v[232:233]
	v_cvt_pk_bf16_f32 v11, v42, v43
	global_store_dwordx4 v[12:13], v[8:11], off
	v_pk_fma_f32 v[38:39], v[4:5], v[136:137], v[230:231]
	s_waitcnt vmcnt(7)
	v_pk_fma_f32 v[32:33], v[2:3], v[130:131], v[236:237]
	v_pk_fma_f32 v[36:37], v[0:1], v[128:129], v[234:235]
	v_cvt_pk_bf16_f32 v0, v38, v39
	v_cvt_pk_bf16_f32 v1, v34, v35
	v_mul_f32_e32 v4, v175, v175
	v_cvt_pk_bf16_f32 v2, v36, v37
	v_cvt_pk_bf16_f32 v3, v32, v33
	global_store_dwordx4 v[12:13], v[0:3], off offset:256
	v_fmac_f32_e32 v4, v174, v174
	v_mul_f32_e32 v5, v179, v179
	v_mul_f32_e32 v3, v177, v177
	v_fmac_f32_e32 v3, v176, v176
	v_add_f32_e32 v3, v3, v4
	v_mul_f32_e32 v4, v181, v181
	v_fmac_f32_e32 v4, v180, v180
	v_fmac_f32_e32 v5, v178, v178
	v_add_f32_e32 v4, v4, v5
	v_mbcnt_lo_u32_b32 v0, -1, 0
	v_add_f32_e32 v3, v3, v4
	v_mul_f32_e32 v4, v167, v167
	v_mul_f32_e32 v5, v165, v165
	v_mbcnt_hi_u32_b32 v1, -1, v0
	v_fmac_f32_e32 v4, v166, v166
	v_fmac_f32_e32 v5, v164, v164
	v_and_b32_e32 v2, 64, v1
	v_add_f32_e32 v4, v4, v5
	v_xor_b32_e32 v0, 16, v1
	v_add_u32_e32 v2, 64, v2
	v_add_f32_e32 v3, v3, v4
	v_mul_f32_e32 v4, v171, v171
	v_mul_f32_e32 v5, v169, v169
	v_cmp_lt_i32_e32 vcc, v0, v2
	v_fmac_f32_e32 v4, v170, v170
	v_fmac_f32_e32 v5, v168, v168
	v_cndmask_b32_e32 v0, v1, v0, vcc
	v_add_f32_e32 v4, v4, v5
	v_lshlrev_b32_e32 v0, 2, v0
	v_add_f32_e32 v3, v3, v4
	v_mov_b32_e32 v4, v3
	s_nop 1
	v_permlane16_swap_b32_e32 v4, v3
	v_xor_b32_e32 v5, 32, v1
	v_cmp_lt_i32_e32 vcc, v5, v2
	s_waitcnt lgkmcnt(0)
	v_add_f32_e32 v3, v3, v4
	v_cndmask_b32_e32 v1, v1, v5, vcc
	v_lshlrev_b32_e32 v2, 2, v1
	v_mov_b32_e32 v4, v3
	s_nop 1
	v_permlane32_swap_b32_e32 v4, v3
	v_cmp_gt_u32_e32 vcc, 16, v187
	v_add_u32_e32 v1, s5, v188
	s_and_saveexec_b64 s[6:7], vcc
	s_cbranch_execz .LBB0_668
	s_waitcnt lgkmcnt(0)
	v_add_f32_e32 v3, v3, v4
	ds_write_b32 v1, v3
.LBB0_668:
	s_or_b64 exec, exec, s[6:7]
	v_mul_f32_e32 v3, v163, v163
	s_waitcnt lgkmcnt(0)
	v_mul_f32_e32 v4, v161, v161
	v_fmac_f32_e32 v3, v162, v162
	v_fmac_f32_e32 v4, v160, v160
	v_add_f32_e32 v3, v3, v4
	v_mul_f32_e32 v4, v157, v157
	v_mul_f32_e32 v5, v159, v159
	v_fmac_f32_e32 v4, v156, v156
	v_fmac_f32_e32 v5, v158, v158
	v_add_f32_e32 v4, v4, v5
	v_add_f32_e32 v3, v3, v4
	v_mul_f32_e32 v4, v155, v155
	v_mul_f32_e32 v5, v151, v151
	v_fmac_f32_e32 v4, v154, v154
	v_fmac_f32_e32 v5, v150, v150
	v_add_f32_e32 v4, v4, v5
	v_add_f32_e32 v3, v3, v4
	v_mul_f32_e32 v4, v153, v153
	v_mul_f32_e32 v5, v149, v149
	v_fmac_f32_e32 v4, v152, v152
	v_fmac_f32_e32 v5, v148, v148
	v_add_f32_e32 v4, v4, v5
	v_add_f32_e32 v3, v3, v4
	v_mov_b32_e32 v4, v3
	s_nop 1
	v_permlane16_swap_b32_e32 v4, v3
	s_waitcnt lgkmcnt(0)
	v_add_f32_e32 v3, v3, v4
	v_mov_b32_e32 v4, v3
	s_nop 1
	v_permlane32_swap_b32_e32 v4, v3
	s_and_saveexec_b64 s[6:7], vcc
	s_cbranch_execz .LBB0_670
	s_waitcnt lgkmcnt(0)
	v_add_f32_e32 v3, v3, v4
	ds_write_b32 v1, v3 offset:256
.LBB0_670:
	s_or_b64 exec, exec, s[6:7]
	v_mul_f32_e32 v3, v127, v127
	s_waitcnt lgkmcnt(0)
	v_mul_f32_e32 v4, v125, v125
	v_fmac_f32_e32 v3, v126, v126
	v_fmac_f32_e32 v4, v124, v124
	v_add_f32_e32 v3, v3, v4
	v_mul_f32_e32 v4, v121, v121
	v_mul_f32_e32 v5, v123, v123
	v_fmac_f32_e32 v4, v120, v120
	v_fmac_f32_e32 v5, v122, v122
	v_add_f32_e32 v4, v4, v5
	v_add_f32_e32 v3, v3, v4
	v_mul_f32_e32 v4, v119, v119
	v_mul_f32_e32 v5, v115, v115
	v_fmac_f32_e32 v4, v118, v118
	v_fmac_f32_e32 v5, v114, v114
	v_add_f32_e32 v4, v4, v5
	v_add_f32_e32 v3, v3, v4
	v_mul_f32_e32 v4, v117, v117
	v_mul_f32_e32 v5, v113, v113
	v_fmac_f32_e32 v4, v116, v116
	v_fmac_f32_e32 v5, v112, v112
	v_add_f32_e32 v4, v4, v5
	v_add_f32_e32 v3, v3, v4
	v_mov_b32_e32 v4, v3
	s_nop 1
	v_permlane16_swap_b32_e32 v4, v3
	s_waitcnt lgkmcnt(0)
	v_add_f32_e32 v3, v3, v4
	v_mov_b32_e32 v4, v3
	s_nop 1
	v_permlane32_swap_b32_e32 v4, v3
	s_and_saveexec_b64 s[6:7], vcc
	s_cbranch_execz .LBB0_672
	s_waitcnt lgkmcnt(0)
	v_add_f32_e32 v3, v3, v4
	ds_write_b32 v1, v3 offset:512
;     __device__ __forceinline__ bool run(const f32x4 (&v)[2][2][4][2], const Unit& u, int wr, int wc, int fr, int fq, PG8_LAS unsigned char* lds, int wid, int lane) const {
;     ...
;             for (int m = 0; m < 4; ++m) { float s = 0.f;
; #pragma unroll
;                 for (int bj = 0; bj < 2; ++bj)
; #pragma unroll
;                     for (int n = 0; n < 2; ++n) { const f32x4 x = v[ai][bj][m][n]; s += (x[0] * x[0] + x[1] * x[1]) + (x[2] * x[2] + x[3] * x[3]); }
;                 s += __shfl_xor(s, 16); s += __shfl_xor(s, 32);
;                 if (fq == 0) P[(ai * HALF + wr * 64 + m * 16 + fr) * 4 + wc] = s; }
.LBB0_672:
	s_or_b64 exec, exec, s[6:7]
	v_mul_f32_e32 v3, v111, v111
	s_waitcnt lgkmcnt(0)
	v_mul_f32_e32 v4, v109, v109
	v_fmac_f32_e32 v3, v110, v110
	v_fmac_f32_e32 v4, v108, v108
	v_add_f32_e32 v3, v3, v4
	v_mul_f32_e32 v4, v105, v105
	v_mul_f32_e32 v5, v107, v107
	v_fmac_f32_e32 v4, v104, v104
	v_fmac_f32_e32 v5, v106, v106
	v_add_f32_e32 v4, v4, v5
	v_add_f32_e32 v3, v3, v4
	v_mul_f32_e32 v4, v95, v95
	v_mul_f32_e32 v5, v91, v91
	v_fmac_f32_e32 v4, v94, v94
	v_fmac_f32_e32 v5, v90, v90
	v_add_f32_e32 v4, v4, v5
	v_add_f32_e32 v3, v3, v4
	v_mul_f32_e32 v4, v93, v93
	v_mul_f32_e32 v5, v89, v89
	v_fmac_f32_e32 v4, v92, v92
	v_fmac_f32_e32 v5, v88, v88
	v_add_f32_e32 v4, v4, v5
	v_add_f32_e32 v3, v3, v4
	v_mov_b32_e32 v4, v3
	s_nop 1
	v_permlane16_swap_b32_e32 v4, v3
	s_waitcnt lgkmcnt(0)
	v_add_f32_e32 v3, v3, v4
	v_mov_b32_e32 v4, v3
	s_nop 1
	v_permlane32_swap_b32_e32 v4, v3
	s_and_saveexec_b64 s[6:7], vcc
	s_cbranch_execz .LBB0_674
	s_waitcnt lgkmcnt(0)
	v_add_f32_e32 v3, v3, v4
	ds_write_b32 v1, v3 offset:768
.LBB0_674:
	s_or_b64 exec, exec, s[6:7]
	v_mul_f32_e32 v3, v103, v103
	s_waitcnt lgkmcnt(0)
	v_mul_f32_e32 v4, v101, v101
	v_fmac_f32_e32 v3, v102, v102
	v_fmac_f32_e32 v4, v100, v100
	v_add_f32_e32 v3, v3, v4
	v_mul_f32_e32 v4, v97, v97
	v_mul_f32_e32 v5, v99, v99
	v_fmac_f32_e32 v4, v96, v96
	v_fmac_f32_e32 v5, v98, v98
	v_add_f32_e32 v4, v4, v5
	v_add_f32_e32 v3, v3, v4
	v_mul_f32_e32 v4, v87, v87
	v_mul_f32_e32 v5, v83, v83
	v_fmac_f32_e32 v4, v86, v86
	v_fmac_f32_e32 v5, v82, v82
	v_add_f32_e32 v4, v4, v5
	v_add_f32_e32 v3, v3, v4
	v_mul_f32_e32 v4, v85, v85
	v_mul_f32_e32 v5, v81, v81
	v_fmac_f32_e32 v4, v84, v84
	v_fmac_f32_e32 v5, v80, v80
	v_add_f32_e32 v4, v4, v5
	v_add_f32_e32 v3, v3, v4
	v_mov_b32_e32 v4, v3
	s_nop 1
	v_permlane16_swap_b32_e32 v4, v3
	s_waitcnt lgkmcnt(0)
	v_add_f32_e32 v3, v3, v4
	v_mov_b32_e32 v4, v3
	s_nop 1
	v_permlane32_swap_b32_e32 v4, v3
	s_and_saveexec_b64 s[6:7], vcc
	s_cbranch_execz .LBB0_676
	s_waitcnt lgkmcnt(0)
	v_add_f32_e32 v3, v3, v4
	ds_write_b32 v1, v3 offset:2048
.LBB0_676:
	s_or_b64 exec, exec, s[6:7]
	v_mul_f32_e32 v3, v79, v79
	s_waitcnt lgkmcnt(0)
	v_mul_f32_e32 v4, v77, v77
	v_fmac_f32_e32 v3, v78, v78
	v_fmac_f32_e32 v4, v76, v76
	v_add_f32_e32 v3, v3, v4
	v_mul_f32_e32 v4, v73, v73
	v_mul_f32_e32 v5, v75, v75
	v_fmac_f32_e32 v4, v72, v72
	v_fmac_f32_e32 v5, v74, v74
	v_add_f32_e32 v4, v4, v5
	v_add_f32_e32 v3, v3, v4
	v_mul_f32_e32 v4, v71, v71
	v_mul_f32_e32 v5, v67, v67
	v_fmac_f32_e32 v4, v70, v70
	v_fmac_f32_e32 v5, v66, v66
	v_add_f32_e32 v4, v4, v5
	v_add_f32_e32 v3, v3, v4
	v_mul_f32_e32 v4, v69, v69
	v_mul_f32_e32 v5, v65, v65
	v_fmac_f32_e32 v4, v68, v68
	v_fmac_f32_e32 v5, v64, v64
	v_add_f32_e32 v4, v4, v5
	v_add_f32_e32 v3, v3, v4
	v_mov_b32_e32 v4, v3
	s_nop 1
	v_permlane16_swap_b32_e32 v4, v3
	s_waitcnt lgkmcnt(0)
	v_add_f32_e32 v3, v3, v4
	v_mov_b32_e32 v4, v3
	s_nop 1
	v_permlane32_swap_b32_e32 v4, v3
	s_and_saveexec_b64 s[6:7], vcc
	s_cbranch_execz .LBB0_678
	s_waitcnt lgkmcnt(0)
	v_add_f32_e32 v3, v3, v4
	ds_write_b32 v1, v3 offset:2304
.LBB0_678:
	s_or_b64 exec, exec, s[6:7]
	v_mul_f32_e32 v3, v63, v63
	s_waitcnt lgkmcnt(0)
	v_mul_f32_e32 v4, v61, v61
	v_fmac_f32_e32 v3, v62, v62
	v_fmac_f32_e32 v4, v60, v60
	v_add_f32_e32 v3, v3, v4
	v_mul_f32_e32 v4, v57, v57
	v_mul_f32_e32 v5, v59, v59
	v_fmac_f32_e32 v4, v56, v56
	v_fmac_f32_e32 v5, v58, v58
	v_add_f32_e32 v4, v4, v5
	v_add_f32_e32 v3, v3, v4
	v_mul_f32_e32 v4, v55, v55
	v_mul_f32_e32 v5, v51, v51
	v_fmac_f32_e32 v4, v54, v54
	v_fmac_f32_e32 v5, v50, v50
	v_add_f32_e32 v4, v4, v5
	v_add_f32_e32 v3, v3, v4
	v_mul_f32_e32 v4, v53, v53
	v_mul_f32_e32 v5, v49, v49
	v_fmac_f32_e32 v4, v52, v52
	v_fmac_f32_e32 v5, v48, v48
	v_add_f32_e32 v4, v4, v5
	v_add_f32_e32 v3, v3, v4
	v_mov_b32_e32 v4, v3
	s_nop 1
	v_permlane16_swap_b32_e32 v4, v3
	s_waitcnt lgkmcnt(0)
	v_add_f32_e32 v3, v3, v4
	v_mov_b32_e32 v4, v3
	s_nop 1
	v_permlane32_swap_b32_e32 v4, v3
	s_and_saveexec_b64 s[6:7], vcc
	s_cbranch_execz .LBB0_680
	s_waitcnt lgkmcnt(0)
	v_add_f32_e32 v3, v3, v4
	ds_write_b32 v1, v3 offset:2560
.LBB0_680:
	s_or_b64 exec, exec, s[6:7]
	v_mul_f32_e32 v3, v47, v47
	s_waitcnt lgkmcnt(0)
	v_mul_f32_e32 v4, v45, v45
	v_fmac_f32_e32 v3, v46, v46
	v_fmac_f32_e32 v4, v44, v44
	v_add_f32_e32 v3, v3, v4
	v_mul_f32_e32 v4, v41, v41
	v_mul_f32_e32 v5, v43, v43
	v_fmac_f32_e32 v4, v40, v40
	v_fmac_f32_e32 v5, v42, v42
	v_add_f32_e32 v4, v4, v5
	v_add_f32_e32 v3, v3, v4
	v_mul_f32_e32 v4, v39, v39
	v_mul_f32_e32 v5, v35, v35
	v_fmac_f32_e32 v4, v38, v38
	v_fmac_f32_e32 v5, v34, v34
	v_add_f32_e32 v4, v4, v5
	v_add_f32_e32 v3, v3, v4
	v_mul_f32_e32 v4, v37, v37
	v_mul_f32_e32 v5, v33, v33
	v_fmac_f32_e32 v4, v36, v36
	v_fmac_f32_e32 v5, v32, v32
	v_add_f32_e32 v4, v4, v5
	v_add_f32_e32 v3, v3, v4
	v_mov_b32_e32 v0, v3
	s_nop 1
	v_permlane16_swap_b32_e32 v0, v3
	s_waitcnt lgkmcnt(0)
	v_add_f32_e32 v0, v3, v0
	v_mov_b32_e32 v2, v0
	s_nop 1
	v_permlane32_swap_b32_e32 v2, v0
	s_and_saveexec_b64 s[6:7], vcc
	s_cbranch_execz .LBB0_682
	s_waitcnt lgkmcnt(0)
	v_add_f32_e32 v0, v0, v2
	ds_write_b32 v1, v0 offset:2816

;     __device__ __forceinline__ void fused(f32x4 (&acc)[2][2][4][2], const Unit& u, int wr, int wc, int fr, int fq, PG8_LAS unsigned char* lds, int wid, int lane) const {
;     ...
;               for (int n = 0; n < 2; ++n) gv[bj][n] = *(const f32x4*)(gate + boff + bj * HALF + n * 4) * asc;
;           bf16_t* op = out + (size_t)row0 * ldc + col0;
;           if constexpr (XF32) {
;               const float* xp = (const float*)xin + (size_t)row0 * ldc + col0; f32x4 xv[4][2][2];
; #pragma unroll
;               for (int ai = 0; ai < 2; ++ai) {
; #pragma unroll
;                   for (int m = 0; m < 4; ++m)
; #pragma unroll
;                       for (int bj = 0; bj < 2; ++bj)
; #pragma unroll
;                           for (int n = 0; n < 2; ++n) xv[m][bj][n] = *(const f32x4*)(xp + (size_t)(ai * HALF + m * 16) * ldc + bj * HALF + n * 4);
; #pragma unroll
;                   for (int m = 0; m < 4; ++m)
; #pragma unroll
;                       for (int bj = 0; bj < 2; ++bj) { acc[ai][bj][m][0] = xv[m][bj][0] + gv[bj][0] * acc[ai][bj][m][0]; acc[ai][bj][m][1] = xv[m][bj][1] + gv[bj][1] * acc[ai][bj][m][1];
;                           *(u32x4*)(op + (size_t)(ai * HALF + m * 16) * ldc + bj * HALF) = pk8(acc[ai][bj][m][0], acc[ai][bj][m][1]); }
;                   asm volatile("" ::: "memory"); }
;           } else {
;               const bf16_t* xp = (const bf16_t*)xin + (size_t)row0 * ldc + col0; u32x4 xw[2][4][2];
; #pragma unroll
;               for (int ai = 0; ai < 2; ++ai)
; #pragma unroll
;                   for (int m = 0; m < 4; ++m)
; #pragma unroll
;                       for (int bj = 0; bj < 2; ++bj) xw[ai][m][bj] = *(const u32x4*)(xp + (size_t)(ai * HALF + m * 16) * ldc + bj * HALF);
; #pragma unroll
;               for (int ai = 0; ai < 2; ++ai)
; #pragma unroll
;                   for (int m = 0; m < 4; ++m)
; #pragma unroll
;                       for (int bj = 0; bj < 2; ++bj) { acc[ai][bj][m][0] = unpk_lo4(xw[ai][m][bj]) + gv[bj][0] * acc[ai][bj][m][0]; acc[ai][bj][m][1] = unpk_hi4(xw[ai][m][bj]) + gv[bj][1] * acc[ai][bj][m][1];
;                           *(u32x4*)(op + (size_t)(ai * HALF + m * 16) * ldc + bj * HALF) = pk8(acc[ai][bj][m][0], acc[ai][bj][m][1]); }
.LBB0_983:
	s_lshl_b32 s6, s42, 5
	v_ashrrev_i32_e32 v0, 1, v203
	s_lshl_b32 s7, s4, 8
	v_and_b32_e32 v0, -8, v0
	s_or_b32 s6, s7, s6
	s_ashr_i32 s8, s3, 31
	v_add_u32_e32 v176, s6, v0
	s_lshr_b32 s6, s8, 20
	s_add_i32 s6, s3, s6
	s_ashr_i32 s6, s6, 12
	v_ashrrev_i32_e32 v177, 31, v176
	v_mov_b32_e32 v0, 0x1800
	v_mad_i64_i32 v[178:179], s[6:7], s6, v0, v[176:177]
	v_lshl_add_u64 v[4:5], v[178:179], 2, s[78:79]
	s_mov_b32 s9, 0x105000
	v_add_co_u32_e32 v0, vcc, s9, v4
	s_barrier
	s_nop 0
	v_addc_co_u32_e32 v1, vcc, 0, v5, vcc
	s_mov_b64 s[6:7], 0x105000
	global_load_dwordx4 v[0:3], v[0:1], off
	v_lshl_add_u64 v[12:13], v[4:5], 0, s[6:7]
	global_load_dwordx4 v[4:7], v[12:13], off offset:16
	global_load_dwordx4 v[8:11], v[12:13], off offset:512
	s_nop 0
	global_load_dwordx4 v[12:15], v[12:13], off offset:528
	v_add_u32_e32 v174, s3, v202
	v_ashrrev_i32_e32 v175, 31, v174
	v_lshlrev_b64 v[16:17], 11, v[174:175]
	v_lshl_add_u64 v[18:19], s[18:19], 0, v[16:17]
	v_lshlrev_b64 v[172:173], 1, v[176:177]
	v_lshl_add_u64 v[196:197], v[18:19], 0, v[172:173]
	global_load_dwordx4 v[180:183], v[196:197], off
	global_load_dwordx4 v[206:209], v[196:197], off offset:256
	s_mov_b32 s13, 0x8000
	v_lshl_add_u64 v[222:223], s[22:23], 0, v[16:17]
	v_add_co_u32_e32 v16, vcc, s13, v196
	s_mov_b32 s12, 0x10000
	s_nop 0
	v_addc_co_u32_e32 v17, vcc, 0, v197, vcc
	global_load_dwordx4 v[210:213], v[16:17], off
	v_add_co_u32_e32 v18, vcc, s12, v196
	s_mov_b32 s11, 0x18000
	s_nop 0
	v_addc_co_u32_e32 v19, vcc, 0, v197, vcc
	v_add_co_u32_e32 v20, vcc, s11, v196
	s_mov_b32 s10, 0x40000
	s_nop 0
	v_addc_co_u32_e32 v21, vcc, 0, v197, vcc
	v_add_co_u32_e32 v22, vcc, s10, v196
	s_mov_b32 s9, 0x48000
	s_nop 0
	v_addc_co_u32_e32 v23, vcc, 0, v197, vcc
	v_add_co_u32_e32 v184, vcc, s9, v196
	s_brev_b32 s6, 60
	s_nop 0
	v_addc_co_u32_e32 v185, vcc, 0, v197, vcc
	global_load_dwordx4 v[214:217], v[16:17], off offset:256
	global_load_dwordx4 v[218:221], v[18:19], off
	global_load_dwordx4 v[168:171], v[18:19], off offset:256
	global_load_dwordx4 v[164:167], v[20:21], off
	global_load_dwordx4 v[160:163], v[20:21], off offset:256
	global_load_dwordx4 v[156:159], v[22:23], off
	global_load_dwordx4 v[152:155], v[22:23], off offset:256
	s_nop 0
	global_load_dwordx4 v[20:23], v[184:185], off
	global_load_dwordx4 v[16:19], v[184:185], off offset:256
	s_mov_b32 s7, 0x50000
	s_lshl_b32 s14, s42, 2
	s_lshl_b32 s5, s5, 10
	s_add_i32 s14, s14, 0
	s_add_i32 s5, s14, s5
	s_waitcnt vmcnt(0)
	v_pk_mul_f32 v[194:195], v[6:7], s[6:7] op_sel_hi:[1,0]
	v_pk_mul_f32 v[198:199], v[0:1], s[6:7] op_sel_hi:[1,0]
	v_add_co_u32_e32 v0, vcc, s7, v196
	v_pk_mul_f32 v[190:191], v[10:11], s[6:7] op_sel_hi:[1,0]
	s_nop 0
	v_addc_co_u32_e32 v1, vcc, 0, v197, vcc
	v_pk_mul_f32 v[188:189], v[8:9], s[6:7] op_sel_hi:[1,0]
	v_pk_mul_f32 v[186:187], v[14:15], s[6:7] op_sel_hi:[1,0]
	v_pk_mul_f32 v[184:185], v[12:13], s[6:7] op_sel_hi:[1,0]
	global_load_dwordx4 v[12:15], v[0:1], off
	global_load_dwordx4 v[8:11], v[0:1], off offset:256
	v_pk_mul_f32 v[200:201], v[2:3], s[6:7] op_sel_hi:[1,0]
	v_pk_mul_f32 v[192:193], v[4:5], s[6:7] op_sel_hi:[1,0]
	s_mov_b32 s6, 0x58000
	v_add_co_u32_e32 v0, vcc, s6, v196
	s_nop 1
	v_addc_co_u32_e32 v1, vcc, 0, v197, vcc
	global_load_dwordx4 v[4:7], v[0:1], off
	s_nop 0
	global_load_dwordx4 v[0:3], v[0:1], off offset:256
	v_lshl_add_u64 v[196:197], v[222:223], 0, v[172:173]
	v_lshlrev_b32_e32 v222, 16, v180
	v_and_b32_e32 v223, 0xffff0000, v180
	v_lshlrev_b32_e32 v180, 16, v181
	v_and_b32_e32 v181, 0xffff0000, v181
	v_pk_fma_f32 v[150:151], v[150:151], v[200:201], v[180:181]
	v_lshlrev_b32_e32 v180, 16, v182
	v_and_b32_e32 v181, 0xffff0000, v182
	v_lshlrev_b32_e32 v182, 16, v183
	v_and_b32_e32 v183, 0xffff0000, v183
	v_pk_fma_f32 v[148:149], v[148:149], v[198:199], v[222:223]
	v_pk_fma_f32 v[146:147], v[146:147], v[194:195], v[182:183]
	v_pk_fma_f32 v[144:145], v[144:145], v[192:193], v[180:181]
	v_cvt_pk_bf16_f32 v180, v148, v149
	v_cvt_pk_bf16_f32 v181, v150, v151
	s_nop 0
	v_cvt_pk_bf16_f32 v182, v144, v145
	v_cvt_pk_bf16_f32 v183, v146, v147
	global_store_dwordx4 v[196:197], v[180:183], off
	s_nop 1
	v_lshlrev_b32_e32 v180, 16, v206
	v_and_b32_e32 v181, 0xffff0000, v206
	v_lshlrev_b32_e32 v182, 16, v207
	v_and_b32_e32 v183, 0xffff0000, v207
	v_pk_fma_f32 v[142:143], v[142:143], v[190:191], v[182:183]
	v_pk_fma_f32 v[140:141], v[140:141], v[188:189], v[180:181]
	v_lshlrev_b32_e32 v182, 16, v208
	v_and_b32_e32 v183, 0xffff0000, v208
	v_lshlrev_b32_e32 v180, 16, v209
	v_and_b32_e32 v181, 0xffff0000, v209
	v_pk_fma_f32 v[180:181], v[134:135], v[186:187], v[180:181]
	v_pk_fma_f32 v[182:183], v[132:133], v[184:185], v[182:183]
	v_cvt_pk_bf16_f32 v132, v140, v141
	v_cvt_pk_bf16_f32 v133, v142, v143
	v_add_co_u32_e32 v206, vcc, s13, v196
	v_cvt_pk_bf16_f32 v134, v182, v183
	v_cvt_pk_bf16_f32 v135, v180, v181
	global_store_dwordx4 v[196:197], v[132:135], off offset:256
	s_nop 0
	v_addc_co_u32_e32 v207, vcc, 0, v197, vcc
	v_lshlrev_b32_e32 v134, 16, v210
	v_and_b32_e32 v135, 0xffff0000, v210
	v_lshlrev_b32_e32 v132, 16, v211
	v_and_b32_e32 v133, 0xffff0000, v211
	v_pk_fma_f32 v[132:133], v[138:139], v[200:201], v[132:133]
	v_pk_fma_f32 v[134:135], v[136:137], v[198:199], v[134:135]
	v_lshlrev_b32_e32 v136, 16, v212
	v_and_b32_e32 v137, 0xffff0000, v212
	v_lshlrev_b32_e32 v138, 16, v213
	v_and_b32_e32 v139, 0xffff0000, v213
	v_pk_fma_f32 v[130:131], v[130:131], v[194:195], v[138:139]
	v_pk_fma_f32 v[128:129], v[128:129], v[192:193], v[136:137]
	v_cvt_pk_bf16_f32 v136, v134, v135
	v_cvt_pk_bf16_f32 v137, v132, v133
	s_nop 0
	v_cvt_pk_bf16_f32 v138, v128, v129
	v_cvt_pk_bf16_f32 v139, v130, v131
; __device__ __forceinline__ f32x4 unpk_lo4(const u32x4 w) { return (f32x4){__uint_as_float(w.x << 16), __uint_as_float(w.x & 0xffff0000u), __uint_as_float(w.y << 16), __uint_as_float(w.y & 0xffff0000u)}; }
; __device__ __forceinline__ f32x4 unpk_hi4(const u32x4 w) { return (f32x4){__uint_as_float(w.z << 16), __uint_as_float(w.z & 0xffff0000u), __uint_as_float(w.w << 16), __uint_as_float(w.w & 0xffff0000u)}; }
; __device__ __forceinline__ u32x4 pk8(const f32x4 a, const f32x4 b) { u32x4 q; q.x = cvt_pk_bf16(a[0], a[1]); q.y = cvt_pk_bf16(a[2], a[3]); q.z = cvt_pk_bf16(b[0], b[1]); q.w = cvt_pk_bf16(b[2], b[3]); return q; }
;     __device__ __forceinline__ void fused(f32x4 (&acc)[2][2][4][2], const Unit& u, int wr, int wc, int fr, int fq, PG8_LAS unsigned char* lds, int wid, int lane) const {
;     ...
; #pragma unroll
;               for (int ai = 0; ai < 2; ++ai)
; #pragma unroll
;                   for (int m = 0; m < 4; ++m)
; #pragma unroll
;                       for (int bj = 0; bj < 2; ++bj) { acc[ai][bj][m][0] = unpk_lo4(xw[ai][m][bj]) + gv[bj][0] * acc[ai][bj][m][0]; acc[ai][bj][m][1] = unpk_hi4(xw[ai][m][bj]) + gv[bj][1] * acc[ai][bj][m][1];
;                           *(u32x4*)(op + (size_t)(ai * HALF + m * 16) * ldc + bj * HALF) = pk8(acc[ai][bj][m][0], acc[ai][bj][m][1]); }
	global_store_dwordx4 v[206:207], v[136:139], off
	s_nop 1
	v_lshlrev_b32_e32 v136, 16, v214
	v_and_b32_e32 v137, 0xffff0000, v214
	v_lshlrev_b32_e32 v138, 16, v215
	v_and_b32_e32 v139, 0xffff0000, v215
	v_pk_fma_f32 v[126:127], v[126:127], v[190:191], v[138:139]
	v_pk_fma_f32 v[124:125], v[124:125], v[188:189], v[136:137]
	v_lshlrev_b32_e32 v138, 16, v216
	v_and_b32_e32 v139, 0xffff0000, v216
	v_lshlrev_b32_e32 v136, 16, v217
	v_and_b32_e32 v137, 0xffff0000, v217
	v_pk_fma_f32 v[136:137], v[118:119], v[186:187], v[136:137]
	v_pk_fma_f32 v[138:139], v[116:117], v[184:185], v[138:139]
	v_cvt_pk_bf16_f32 v116, v124, v125
	v_cvt_pk_bf16_f32 v117, v126, v127
	s_nop 0
	v_cvt_pk_bf16_f32 v118, v138, v139
	v_cvt_pk_bf16_f32 v119, v136, v137
	global_store_dwordx4 v[206:207], v[116:119], off offset:256
	v_add_co_u32_e32 v206, vcc, s12, v196
	s_nop 0
	v_lshlrev_b32_e32 v118, 16, v218
	v_and_b32_e32 v119, 0xffff0000, v218
	v_lshlrev_b32_e32 v116, 16, v219
	v_and_b32_e32 v117, 0xffff0000, v219
	v_pk_fma_f32 v[116:117], v[122:123], v[200:201], v[116:117]
	v_pk_fma_f32 v[118:119], v[120:121], v[198:199], v[118:119]
	v_lshlrev_b32_e32 v120, 16, v220
	v_and_b32_e32 v121, 0xffff0000, v220
	v_lshlrev_b32_e32 v122, 16, v221
	v_and_b32_e32 v123, 0xffff0000, v221
	v_pk_fma_f32 v[114:115], v[114:115], v[194:195], v[122:123]
	v_pk_fma_f32 v[112:113], v[112:113], v[192:193], v[120:121]
	v_cvt_pk_bf16_f32 v120, v118, v119
	v_cvt_pk_bf16_f32 v121, v116, v117
	v_addc_co_u32_e32 v207, vcc, 0, v197, vcc
	v_cvt_pk_bf16_f32 v122, v112, v113
	v_cvt_pk_bf16_f32 v123, v114, v115
	global_store_dwordx4 v[206:207], v[120:123], off
	s_nop 1
	v_lshlrev_b32_e32 v120, 16, v168
	v_and_b32_e32 v121, 0xffff0000, v168
	v_lshlrev_b32_e32 v122, 16, v169
	v_and_b32_e32 v123, 0xffff0000, v169
	v_pk_fma_f32 v[110:111], v[110:111], v[190:191], v[122:123]
	v_pk_fma_f32 v[108:109], v[108:109], v[188:189], v[120:121]
	v_lshlrev_b32_e32 v122, 16, v170
	v_and_b32_e32 v123, 0xffff0000, v170
	v_lshlrev_b32_e32 v120, 16, v171
	v_and_b32_e32 v121, 0xffff0000, v171
	v_pk_fma_f32 v[120:121], v[102:103], v[186:187], v[120:121]
	v_pk_fma_f32 v[122:123], v[100:101], v[184:185], v[122:123]
	v_cvt_pk_bf16_f32 v100, v108, v109
	v_cvt_pk_bf16_f32 v101, v110, v111
	s_nop 0
	v_cvt_pk_bf16_f32 v102, v122, v123
	v_cvt_pk_bf16_f32 v103, v120, v121
	global_store_dwordx4 v[206:207], v[100:103], off offset:256
	s_nop 1
	v_lshlrev_b32_e32 v102, 16, v164
	v_and_b32_e32 v103, 0xffff0000, v164
	v_lshlrev_b32_e32 v100, 16, v165
	v_and_b32_e32 v101, 0xffff0000, v165
	v_pk_fma_f32 v[102:103], v[104:105], v[198:199], v[102:103]
	v_lshlrev_b32_e32 v104, 16, v166
	v_and_b32_e32 v105, 0xffff0000, v166
	v_add_co_u32_e32 v164, vcc, s11, v196
	v_pk_fma_f32 v[100:101], v[106:107], v[200:201], v[100:101]
	v_lshlrev_b32_e32 v106, 16, v167
	v_and_b32_e32 v107, 0xffff0000, v167
	v_pk_fma_f32 v[96:97], v[96:97], v[192:193], v[104:105]
	v_cvt_pk_bf16_f32 v104, v102, v103
	v_cvt_pk_bf16_f32 v105, v100, v101
	v_addc_co_u32_e32 v165, vcc, 0, v197, vcc
	v_pk_fma_f32 v[98:99], v[98:99], v[194:195], v[106:107]
	v_cvt_pk_bf16_f32 v106, v96, v97
	s_nop 0
	v_cvt_pk_bf16_f32 v107, v98, v99
	global_store_dwordx4 v[164:165], v[104:107], off
	s_nop 1
	v_lshlrev_b32_e32 v104, 16, v160
	v_and_b32_e32 v105, 0xffff0000, v160
	v_lshlrev_b32_e32 v106, 16, v161
	v_and_b32_e32 v107, 0xffff0000, v161
	v_pk_fma_f32 v[92:93], v[92:93], v[188:189], v[104:105]
	v_lshlrev_b32_e32 v104, 16, v162
	v_and_b32_e32 v105, 0xffff0000, v162
	v_pk_fma_f32 v[94:95], v[94:95], v[190:191], v[106:107]
	v_lshlrev_b32_e32 v106, 16, v163
	v_and_b32_e32 v107, 0xffff0000, v163
	v_pk_fma_f32 v[88:89], v[88:89], v[184:185], v[104:105]
	v_cvt_pk_bf16_f32 v104, v92, v93
	v_cvt_pk_bf16_f32 v105, v94, v95
	v_pk_fma_f32 v[90:91], v[90:91], v[186:187], v[106:107]
	v_cvt_pk_bf16_f32 v106, v88, v89
	s_nop 0
	v_cvt_pk_bf16_f32 v107, v90, v91
	global_store_dwordx4 v[164:165], v[104:107], off offset:256
	s_nop 1
	v_lshlrev_b32_e32 v104, 16, v156
	v_and_b32_e32 v105, 0xffff0000, v156
	v_lshlrev_b32_e32 v106, 16, v157
	v_and_b32_e32 v107, 0xffff0000, v157
	v_pk_fma_f32 v[84:85], v[84:85], v[198:199], v[104:105]
	v_lshlrev_b32_e32 v104, 16, v158
	v_and_b32_e32 v105, 0xffff0000, v158
	v_add_co_u32_e32 v156, vcc, s10, v196
	v_pk_fma_f32 v[86:87], v[86:87], v[200:201], v[106:107]
	v_lshlrev_b32_e32 v106, 16, v159
	v_and_b32_e32 v107, 0xffff0000, v159
	v_pk_fma_f32 v[80:81], v[80:81], v[192:193], v[104:105]
	v_cvt_pk_bf16_f32 v104, v84, v85
	v_cvt_pk_bf16_f32 v105, v86, v87
	v_addc_co_u32_e32 v157, vcc, 0, v197, vcc
	v_pk_fma_f32 v[82:83], v[82:83], v[194:195], v[106:107]
	v_cvt_pk_bf16_f32 v106, v80, v81
	s_nop 0
	v_cvt_pk_bf16_f32 v107, v82, v83
	global_store_dwordx4 v[156:157], v[104:107], off
	s_nop 1
	v_lshlrev_b32_e32 v104, 16, v152
	v_and_b32_e32 v105, 0xffff0000, v152
	v_lshlrev_b32_e32 v106, 16, v153
	v_and_b32_e32 v107, 0xffff0000, v153
	v_pk_fma_f32 v[76:77], v[76:77], v[188:189], v[104:105]
	v_lshlrev_b32_e32 v104, 16, v154
	v_and_b32_e32 v105, 0xffff0000, v154
	v_pk_fma_f32 v[78:79], v[78:79], v[190:191], v[106:107]
	v_lshlrev_b32_e32 v106, 16, v155
	v_and_b32_e32 v107, 0xffff0000, v155
	v_pk_fma_f32 v[104:105], v[68:69], v[184:185], v[104:105]
	v_lshlrev_b32_e32 v68, 16, v20
	v_and_b32_e32 v69, 0xffff0000, v20
	v_pk_fma_f32 v[70:71], v[70:71], v[186:187], v[106:107]
	v_lshlrev_b32_e32 v20, 16, v21
	v_and_b32_e32 v21, 0xffff0000, v21
	v_pk_fma_f32 v[68:69], v[72:73], v[198:199], v[68:69]
	v_lshlrev_b32_e32 v72, 16, v22
	v_and_b32_e32 v73, 0xffff0000, v22
	v_add_co_u32_e32 v106, vcc, s9, v196
	v_cvt_pk_bf16_f32 v152, v76, v77
	v_cvt_pk_bf16_f32 v153, v78, v79
	v_cvt_pk_bf16_f32 v154, v104, v105
	v_cvt_pk_bf16_f32 v155, v70, v71
	global_store_dwordx4 v[156:157], v[152:155], off offset:256
	v_pk_fma_f32 v[20:21], v[74:75], v[200:201], v[20:21]
	v_lshlrev_b32_e32 v22, 16, v23
	v_and_b32_e32 v23, 0xffff0000, v23
	v_pk_fma_f32 v[64:65], v[64:65], v[192:193], v[72:73]
	v_cvt_pk_bf16_f32 v72, v68, v69
	v_cvt_pk_bf16_f32 v73, v20, v21
	v_addc_co_u32_e32 v107, vcc, 0, v197, vcc
	v_pk_fma_f32 v[66:67], v[66:67], v[194:195], v[22:23]
	v_cvt_pk_bf16_f32 v74, v64, v65
	s_nop 0
	v_cvt_pk_bf16_f32 v75, v66, v67
	global_store_dwordx4 v[106:107], v[72:75], off
	s_nop 1
	v_lshlrev_b32_e32 v72, 16, v16
	v_and_b32_e32 v73, 0xffff0000, v16
	v_lshlrev_b32_e32 v16, 16, v17
	v_and_b32_e32 v17, 0xffff0000, v17
	v_pk_fma_f32 v[22:23], v[62:63], v[190:191], v[16:17]
	v_lshlrev_b32_e32 v16, 16, v18
	v_and_b32_e32 v17, 0xffff0000, v18
	v_lshlrev_b32_e32 v18, 16, v19
	v_and_b32_e32 v19, 0xffff0000, v19
	v_pk_fma_f32 v[60:61], v[60:61], v[188:189], v[72:73]
	v_pk_fma_f32 v[54:55], v[54:55], v[186:187], v[18:19]
	v_pk_fma_f32 v[52:53], v[52:53], v[184:185], v[16:17]
	v_cvt_pk_bf16_f32 v16, v60, v61
	v_cvt_pk_bf16_f32 v17, v22, v23
	v_add_co_u32_e32 v62, vcc, s7, v196
	v_cvt_pk_bf16_f32 v18, v52, v53
	v_cvt_pk_bf16_f32 v19, v54, v55
	global_store_dwordx4 v[106:107], v[16:19], off offset:256
	s_nop 0
	v_addc_co_u32_e32 v63, vcc, 0, v197, vcc
	s_waitcnt vmcnt(15)
; __device__ __forceinline__ f32x4 unpk_lo4(const u32x4 w) { return (f32x4){__uint_as_float(w.x << 16), __uint_as_float(w.x & 0xffff0000u), __uint_as_float(w.y << 16), __uint_as_float(w.y & 0xffff0000u)}; }
; __device__ __forceinline__ f32x4 unpk_hi4(const u32x4 w) { return (f32x4){__uint_as_float(w.z << 16), __uint_as_float(w.z & 0xffff0000u), __uint_as_float(w.w << 16), __uint_as_float(w.w & 0xffff0000u)}; }
; __device__ __forceinline__ u32x4 pk8(const f32x4 a, const f32x4 b) { u32x4 q; q.x = cvt_pk_bf16(a[0], a[1]); q.y = cvt_pk_bf16(a[2], a[3]); q.z = cvt_pk_bf16(b[0], b[1]); q.w = cvt_pk_bf16(b[2], b[3]); return q; }
;     __device__ __forceinline__ bool run(const f32x4 (&v)[2][2][4][2], const Unit& u, int wr, int wc, int fr, int fq, PG8_LAS unsigned char* lds, int wid, int lane) const {
;     ...
;             for (int m = 0; m < 4; ++m) { float s = 0.f;
; #pragma unroll
;                 for (int bj = 0; bj < 2; ++bj)
; #pragma unroll
;                     for (int n = 0; n < 2; ++n) { const f32x4 x = v[ai][bj][m][n]; s += (x[0] * x[0] + x[1] * x[1]) + (x[2] * x[2] + x[3] * x[3]); }
;                 s += __shfl_xor(s, 16); s += __shfl_xor(s, 32);
;                 if (fq == 0) P[(ai * HALF + wr * 64 + m * 16 + fr) * 4 + wc] = s; }
;     __device__ __forceinline__ void fused(f32x4 (&acc)[2][2][4][2], const Unit& u, int wr, int wc, int fr, int fq, PG8_LAS unsigned char* lds, int wid, int lane) const {
;     ...
; #pragma unroll
;               for (int ai = 0; ai < 2; ++ai)
; #pragma unroll
;                   for (int m = 0; m < 4; ++m)
; #pragma unroll
;                       for (int bj = 0; bj < 2; ++bj) { acc[ai][bj][m][0] = unpk_lo4(xw[ai][m][bj]) + gv[bj][0] * acc[ai][bj][m][0]; acc[ai][bj][m][1] = unpk_hi4(xw[ai][m][bj]) + gv[bj][1] * acc[ai][bj][m][1];
;                           *(u32x4*)(op + (size_t)(ai * HALF + m * 16) * ldc + bj * HALF) = pk8(acc[ai][bj][m][0], acc[ai][bj][m][1]); }
	v_lshlrev_b32_e32 v18, 16, v12
	v_and_b32_e32 v19, 0xffff0000, v12
	v_lshlrev_b32_e32 v12, 16, v13
	v_and_b32_e32 v13, 0xffff0000, v13
	v_pk_fma_f32 v[16:17], v[58:59], v[200:201], v[12:13]
	v_lshlrev_b32_e32 v12, 16, v14
	v_and_b32_e32 v13, 0xffff0000, v14
	v_pk_fma_f32 v[18:19], v[56:57], v[198:199], v[18:19]
	v_lshlrev_b32_e32 v14, 16, v15
	v_and_b32_e32 v15, 0xffff0000, v15
	v_pk_fma_f32 v[48:49], v[48:49], v[192:193], v[12:13]
	v_cvt_pk_bf16_f32 v12, v18, v19
	v_cvt_pk_bf16_f32 v13, v16, v17
	v_pk_fma_f32 v[50:51], v[50:51], v[194:195], v[14:15]
	v_cvt_pk_bf16_f32 v14, v48, v49
	s_nop 0
	v_cvt_pk_bf16_f32 v15, v50, v51
	global_store_dwordx4 v[62:63], v[12:15], off
	s_waitcnt vmcnt(15)
	s_nop 0
	v_lshlrev_b32_e32 v12, 16, v8
	v_and_b32_e32 v13, 0xffff0000, v8
	v_lshlrev_b32_e32 v8, 16, v9
	v_and_b32_e32 v9, 0xffff0000, v9
	v_pk_fma_f32 v[46:47], v[46:47], v[190:191], v[8:9]
	v_lshlrev_b32_e32 v8, 16, v10
	v_and_b32_e32 v9, 0xffff0000, v10
	v_pk_fma_f32 v[44:45], v[44:45], v[188:189], v[12:13]
	v_lshlrev_b32_e32 v10, 16, v11
	v_and_b32_e32 v11, 0xffff0000, v11
	v_pk_fma_f32 v[58:59], v[36:37], v[184:185], v[8:9]
	v_cvt_pk_bf16_f32 v8, v44, v45
	v_cvt_pk_bf16_f32 v9, v46, v47
	v_pk_fma_f32 v[56:57], v[38:39], v[186:187], v[10:11]
	v_cvt_pk_bf16_f32 v10, v58, v59
	s_nop 0
	v_cvt_pk_bf16_f32 v11, v56, v57
	global_store_dwordx4 v[62:63], v[8:11], off offset:256
	s_waitcnt vmcnt(15)
	s_nop 0
	v_lshlrev_b32_e32 v8, 16, v4
	v_and_b32_e32 v9, 0xffff0000, v4
	v_lshlrev_b32_e32 v4, 16, v5
	v_and_b32_e32 v5, 0xffff0000, v5
	v_pk_fma_f32 v[36:37], v[42:43], v[200:201], v[4:5]
	v_pk_fma_f32 v[38:39], v[40:41], v[198:199], v[8:9]
	v_lshlrev_b32_e32 v4, 16, v6
	v_and_b32_e32 v5, 0xffff0000, v6
	v_add_co_u32_e32 v8, vcc, s6, v196
	v_lshlrev_b32_e32 v6, 16, v7
	v_and_b32_e32 v7, 0xffff0000, v7
	v_pk_fma_f32 v[32:33], v[32:33], v[192:193], v[4:5]
	v_cvt_pk_bf16_f32 v4, v38, v39
	v_cvt_pk_bf16_f32 v5, v36, v37
	v_addc_co_u32_e32 v9, vcc, 0, v197, vcc
	v_pk_fma_f32 v[34:35], v[34:35], v[194:195], v[6:7]
	v_cvt_pk_bf16_f32 v6, v32, v33
	s_nop 0
	v_cvt_pk_bf16_f32 v7, v34, v35
	global_store_dwordx4 v[8:9], v[4:7], off
	s_waitcnt vmcnt(15)
	s_nop 0
	v_lshlrev_b32_e32 v4, 16, v0
	v_and_b32_e32 v5, 0xffff0000, v0
	v_lshlrev_b32_e32 v0, 16, v1
	v_and_b32_e32 v1, 0xffff0000, v1
	v_pk_fma_f32 v[30:31], v[30:31], v[190:191], v[0:1]
	v_lshlrev_b32_e32 v0, 16, v2
	v_and_b32_e32 v1, 0xffff0000, v2
	v_lshlrev_b32_e32 v2, 16, v3
	v_and_b32_e32 v3, 0xffff0000, v3
	v_pk_fma_f32 v[28:29], v[28:29], v[188:189], v[4:5]
	v_pk_fma_f32 v[26:27], v[26:27], v[186:187], v[2:3]
	v_pk_fma_f32 v[24:25], v[24:25], v[184:185], v[0:1]
	v_cvt_pk_bf16_f32 v0, v28, v29
	v_cvt_pk_bf16_f32 v1, v30, v31
	v_mul_f32_e32 v4, v151, v151
	v_cvt_pk_bf16_f32 v2, v24, v25
	v_cvt_pk_bf16_f32 v3, v26, v27
	global_store_dwordx4 v[8:9], v[0:3], off offset:256
	v_fmac_f32_e32 v4, v150, v150
	v_mul_f32_e32 v5, v147, v147
	v_mul_f32_e32 v3, v149, v149
	v_fmac_f32_e32 v3, v148, v148
	v_add_f32_e32 v3, v3, v4
	v_mul_f32_e32 v4, v145, v145
	v_fmac_f32_e32 v4, v144, v144
	v_fmac_f32_e32 v5, v146, v146
	v_add_f32_e32 v4, v4, v5
	v_mbcnt_lo_u32_b32 v0, -1, 0
	v_add_f32_e32 v3, v3, v4
	v_mul_f32_e32 v4, v141, v141
	v_mul_f32_e32 v5, v143, v143
	v_mbcnt_hi_u32_b32 v1, -1, v0
	v_fmac_f32_e32 v4, v140, v140
	v_fmac_f32_e32 v5, v142, v142
	v_and_b32_e32 v2, 64, v1
	v_add_f32_e32 v4, v4, v5
	v_xor_b32_e32 v0, 16, v1
	v_add_u32_e32 v2, 64, v2
	v_add_f32_e32 v3, v3, v4
	v_mul_f32_e32 v4, v183, v183
	v_mul_f32_e32 v5, v181, v181
	v_cmp_lt_i32_e32 vcc, v0, v2
	v_fmac_f32_e32 v4, v182, v182
	v_fmac_f32_e32 v5, v180, v180
	v_cndmask_b32_e32 v0, v1, v0, vcc
	v_add_f32_e32 v4, v4, v5
	v_lshlrev_b32_e32 v0, 2, v0
	v_add_f32_e32 v3, v4, v3
	v_mov_b32_e32 v4, v3
	s_nop 1
	v_permlane16_swap_b32_e32 v4, v3
	v_xor_b32_e32 v5, 32, v1
	v_cmp_lt_i32_e32 vcc, v5, v2
	s_waitcnt lgkmcnt(0)
	v_add_f32_e32 v3, v3, v4
	v_cndmask_b32_e32 v1, v1, v5, vcc
	v_lshlrev_b32_e32 v2, 2, v1
	v_mov_b32_e32 v4, v3
	s_nop 1
	v_permlane32_swap_b32_e32 v4, v3
	v_cmp_gt_u32_e32 vcc, 16, v203
	v_add_u32_e32 v1, s5, v204
	s_and_saveexec_b64 s[6:7], vcc
	v_readlane_b32 s44, v254, 36
	v_readlane_b32 s56, v254, 48
	v_readlane_b32 s57, v254, 49
	v_readlane_b32 s58, v254, 50
	v_readlane_b32 s59, v254, 51
	v_readlane_b32 s52, v254, 44
	v_readlane_b32 s53, v254, 45
	v_readlane_b32 s54, v254, 46
	v_readlane_b32 s55, v254, 47
	s_mov_b64 s[62:63], s[58:59]
	s_mov_b64 s[60:61], s[56:57]
	s_mov_b64 s[58:59], s[54:55]
	s_mov_b64 s[56:57], s[52:53]
	v_readlane_b32 s45, v254, 37
	v_readlane_b32 s46, v254, 38
	v_readlane_b32 s47, v254, 39
	v_readlane_b32 s48, v254, 40
	v_readlane_b32 s49, v254, 41
	v_readlane_b32 s50, v254, 42
	v_readlane_b32 s51, v254, 43
	s_cbranch_execz .LBB0_985
	s_waitcnt lgkmcnt(0)
	v_add_f32_e32 v3, v3, v4
	ds_write_b32 v1, v3
.LBB0_985:
	s_or_b64 exec, exec, s[6:7]
	v_mul_f32_e32 v3, v135, v135
	s_waitcnt lgkmcnt(0)
	v_mul_f32_e32 v4, v133, v133
	v_fmac_f32_e32 v3, v134, v134
	v_fmac_f32_e32 v4, v132, v132
	v_add_f32_e32 v3, v3, v4
	v_mul_f32_e32 v4, v129, v129
	v_mul_f32_e32 v5, v131, v131
	v_fmac_f32_e32 v4, v128, v128
	v_fmac_f32_e32 v5, v130, v130
	v_add_f32_e32 v4, v4, v5
	v_add_f32_e32 v3, v3, v4
	v_mul_f32_e32 v4, v125, v125
	v_mul_f32_e32 v5, v127, v127
	v_fmac_f32_e32 v4, v124, v124
	v_fmac_f32_e32 v5, v126, v126
	v_add_f32_e32 v4, v4, v5
	v_add_f32_e32 v3, v3, v4
	v_mul_f32_e32 v4, v139, v139
	v_mul_f32_e32 v5, v137, v137
	v_fmac_f32_e32 v4, v138, v138
	v_fmac_f32_e32 v5, v136, v136
	v_add_f32_e32 v4, v4, v5
	v_add_f32_e32 v3, v4, v3
	v_mov_b32_e32 v4, v3
	s_nop 1
	v_permlane16_swap_b32_e32 v4, v3
	s_waitcnt lgkmcnt(0)
	v_add_f32_e32 v3, v3, v4
	v_mov_b32_e32 v4, v3
	s_nop 1
	v_permlane32_swap_b32_e32 v4, v3
	s_and_saveexec_b64 s[6:7], vcc
	s_cbranch_execz .LBB0_987
	s_waitcnt lgkmcnt(0)
	v_add_f32_e32 v3, v3, v4
	ds_write_b32 v1, v3 offset:256
;     __device__ __forceinline__ bool run(const f32x4 (&v)[2][2][4][2], const Unit& u, int wr, int wc, int fr, int fq, PG8_LAS unsigned char* lds, int wid, int lane) const {
;     ...
;             for (int m = 0; m < 4; ++m) { float s = 0.f;
; #pragma unroll
;                 for (int bj = 0; bj < 2; ++bj)
; #pragma unroll
;                     for (int n = 0; n < 2; ++n) { const f32x4 x = v[ai][bj][m][n]; s += (x[0] * x[0] + x[1] * x[1]) + (x[2] * x[2] + x[3] * x[3]); }
;                 s += __shfl_xor(s, 16); s += __shfl_xor(s, 32);
;                 if (fq == 0) P[(ai * HALF + wr * 64 + m * 16 + fr) * 4 + wc] = s; }
.LBB0_987:
	s_or_b64 exec, exec, s[6:7]
	v_mul_f32_e32 v3, v119, v119
	s_waitcnt lgkmcnt(0)
	v_mul_f32_e32 v4, v117, v117
	v_fmac_f32_e32 v3, v118, v118
	v_fmac_f32_e32 v4, v116, v116
	v_add_f32_e32 v3, v3, v4
	v_mul_f32_e32 v4, v113, v113
	v_mul_f32_e32 v5, v115, v115
	v_fmac_f32_e32 v4, v112, v112
	v_fmac_f32_e32 v5, v114, v114
	v_add_f32_e32 v4, v4, v5
	v_add_f32_e32 v3, v3, v4
	v_mul_f32_e32 v4, v109, v109
	v_mul_f32_e32 v5, v111, v111
	v_fmac_f32_e32 v4, v108, v108
	v_fmac_f32_e32 v5, v110, v110
	v_add_f32_e32 v4, v4, v5
	v_add_f32_e32 v3, v3, v4
	v_mul_f32_e32 v4, v123, v123
	v_mul_f32_e32 v5, v121, v121
	v_fmac_f32_e32 v4, v122, v122
	v_fmac_f32_e32 v5, v120, v120
	v_add_f32_e32 v4, v4, v5
	v_add_f32_e32 v3, v4, v3
	v_mov_b32_e32 v4, v3
	s_nop 1
	v_permlane16_swap_b32_e32 v4, v3
	s_waitcnt lgkmcnt(0)
	v_add_f32_e32 v3, v3, v4
	v_mov_b32_e32 v4, v3
	s_nop 1
	v_permlane32_swap_b32_e32 v4, v3
	s_and_saveexec_b64 s[6:7], vcc
	s_cbranch_execz .LBB0_989
	s_waitcnt lgkmcnt(0)
	v_add_f32_e32 v3, v3, v4
	ds_write_b32 v1, v3 offset:512
.LBB0_989:
	s_or_b64 exec, exec, s[6:7]
	v_mul_f32_e32 v3, v103, v103
	s_waitcnt lgkmcnt(0)
	v_mul_f32_e32 v4, v101, v101
	v_fmac_f32_e32 v3, v102, v102
	v_fmac_f32_e32 v4, v100, v100
	v_add_f32_e32 v3, v3, v4
	v_mul_f32_e32 v4, v97, v97
	v_mul_f32_e32 v5, v99, v99
	v_fmac_f32_e32 v4, v96, v96
	v_fmac_f32_e32 v5, v98, v98
	v_add_f32_e32 v4, v4, v5
	v_add_f32_e32 v3, v3, v4
	v_mul_f32_e32 v4, v93, v93
	v_mul_f32_e32 v5, v95, v95
	v_fmac_f32_e32 v4, v92, v92
	v_fmac_f32_e32 v5, v94, v94
	v_add_f32_e32 v4, v4, v5
	v_add_f32_e32 v3, v3, v4
	v_mul_f32_e32 v4, v89, v89
	v_mul_f32_e32 v5, v91, v91
	v_fmac_f32_e32 v4, v88, v88
	v_fmac_f32_e32 v5, v90, v90
	v_add_f32_e32 v4, v4, v5
	v_add_f32_e32 v3, v4, v3
	v_mov_b32_e32 v4, v3
	s_nop 1
	v_permlane16_swap_b32_e32 v4, v3
	s_waitcnt lgkmcnt(0)
	v_add_f32_e32 v3, v3, v4
	v_mov_b32_e32 v4, v3
	s_nop 1
	v_permlane32_swap_b32_e32 v4, v3
	s_and_saveexec_b64 s[6:7], vcc
	s_cbranch_execz .LBB0_991
	s_waitcnt lgkmcnt(0)
	v_add_f32_e32 v3, v3, v4
	ds_write_b32 v1, v3 offset:768
.LBB0_991:
	s_or_b64 exec, exec, s[6:7]
	v_mul_f32_e32 v3, v85, v85
	s_waitcnt lgkmcnt(0)
	v_mul_f32_e32 v4, v87, v87
	v_fmac_f32_e32 v3, v84, v84
	v_fmac_f32_e32 v4, v86, v86
	v_add_f32_e32 v3, v3, v4
	v_mul_f32_e32 v4, v81, v81
	v_mul_f32_e32 v5, v83, v83
	v_fmac_f32_e32 v4, v80, v80
	v_fmac_f32_e32 v5, v82, v82
	v_add_f32_e32 v4, v4, v5
	v_add_f32_e32 v3, v3, v4
	v_mul_f32_e32 v4, v77, v77
	v_mul_f32_e32 v5, v79, v79
	v_fmac_f32_e32 v4, v76, v76
	v_fmac_f32_e32 v5, v78, v78
	v_add_f32_e32 v4, v4, v5
	v_add_f32_e32 v3, v3, v4
	v_mul_f32_e32 v4, v105, v105
	v_mul_f32_e32 v5, v71, v71
	v_fmac_f32_e32 v4, v104, v104
	v_fmac_f32_e32 v5, v70, v70
	v_add_f32_e32 v4, v4, v5
	v_add_f32_e32 v3, v4, v3
	v_mov_b32_e32 v4, v3
	s_nop 1
	v_permlane16_swap_b32_e32 v4, v3
	s_waitcnt lgkmcnt(0)
	v_add_f32_e32 v3, v3, v4
	v_mov_b32_e32 v4, v3
	s_nop 1
	v_permlane32_swap_b32_e32 v4, v3
	s_and_saveexec_b64 s[6:7], vcc
	s_cbranch_execz .LBB0_993
	s_waitcnt lgkmcnt(0)
	v_add_f32_e32 v3, v3, v4
	ds_write_b32 v1, v3 offset:2048
.LBB0_993:
	s_or_b64 exec, exec, s[6:7]
	v_mul_f32_e32 v3, v69, v69
	s_waitcnt lgkmcnt(0)
	v_mul_f32_e32 v4, v21, v21
	v_fmac_f32_e32 v3, v68, v68
	v_fmac_f32_e32 v4, v20, v20
	v_add_f32_e32 v3, v3, v4
	v_mul_f32_e32 v4, v65, v65
	v_mul_f32_e32 v5, v67, v67
	v_fmac_f32_e32 v4, v64, v64
	v_fmac_f32_e32 v5, v66, v66
	v_add_f32_e32 v4, v4, v5
	v_add_f32_e32 v3, v3, v4
	v_mul_f32_e32 v4, v61, v61
	v_mul_f32_e32 v5, v23, v23
	v_fmac_f32_e32 v4, v60, v60
	v_fmac_f32_e32 v5, v22, v22
	v_add_f32_e32 v4, v4, v5
	v_add_f32_e32 v3, v3, v4
	v_mul_f32_e32 v4, v53, v53
	v_mul_f32_e32 v5, v55, v55
	v_fmac_f32_e32 v4, v52, v52
	v_fmac_f32_e32 v5, v54, v54
	v_add_f32_e32 v4, v4, v5
	v_add_f32_e32 v3, v4, v3
	v_mov_b32_e32 v4, v3
	s_nop 1
	v_permlane16_swap_b32_e32 v4, v3
	s_waitcnt lgkmcnt(0)
	v_add_f32_e32 v3, v3, v4
	v_mov_b32_e32 v4, v3
	s_nop 1
	v_permlane32_swap_b32_e32 v4, v3
	s_and_saveexec_b64 s[6:7], vcc
	s_cbranch_execz .LBB0_995
	s_waitcnt lgkmcnt(0)
	v_add_f32_e32 v3, v3, v4
	ds_write_b32 v1, v3 offset:2304
.LBB0_995:
	s_or_b64 exec, exec, s[6:7]
	v_mul_f32_e32 v3, v19, v19
	s_waitcnt lgkmcnt(0)
	v_mul_f32_e32 v4, v17, v17
	v_fmac_f32_e32 v3, v18, v18
	v_fmac_f32_e32 v4, v16, v16
	v_add_f32_e32 v3, v3, v4
	v_mul_f32_e32 v4, v49, v49
	v_mul_f32_e32 v5, v51, v51
	v_fmac_f32_e32 v4, v48, v48
	v_fmac_f32_e32 v5, v50, v50
	v_add_f32_e32 v4, v4, v5
	v_add_f32_e32 v3, v3, v4
	v_mul_f32_e32 v4, v45, v45
	v_mul_f32_e32 v5, v47, v47
	v_fmac_f32_e32 v4, v44, v44
	v_fmac_f32_e32 v5, v46, v46
	v_add_f32_e32 v4, v4, v5
	v_add_f32_e32 v3, v3, v4
	v_mul_f32_e32 v4, v59, v59
	v_mul_f32_e32 v5, v57, v57
	v_fmac_f32_e32 v4, v58, v58
	v_fmac_f32_e32 v5, v56, v56
	v_add_f32_e32 v4, v4, v5
	v_add_f32_e32 v3, v4, v3
	v_mov_b32_e32 v4, v3
	s_nop 1
	v_permlane16_swap_b32_e32 v4, v3
	s_waitcnt lgkmcnt(0)
	v_add_f32_e32 v3, v3, v4
	v_mov_b32_e32 v4, v3
	s_nop 1
	v_permlane32_swap_b32_e32 v4, v3
	s_and_saveexec_b64 s[6:7], vcc
	s_cbranch_execz .LBB0_997
	s_waitcnt lgkmcnt(0)
	v_add_f32_e32 v3, v3, v4
	ds_write_b32 v1, v3 offset:2560
.LBB0_997:
	s_or_b64 exec, exec, s[6:7]
	v_mul_f32_e32 v3, v39, v39
	s_waitcnt lgkmcnt(0)
	v_mul_f32_e32 v4, v37, v37
	v_fmac_f32_e32 v3, v38, v38
	v_fmac_f32_e32 v4, v36, v36
	v_add_f32_e32 v3, v3, v4
	v_mul_f32_e32 v4, v33, v33
	v_mul_f32_e32 v5, v35, v35
	v_fmac_f32_e32 v4, v32, v32
	v_fmac_f32_e32 v5, v34, v34
	v_add_f32_e32 v4, v4, v5
	v_add_f32_e32 v3, v3, v4
	v_mul_f32_e32 v4, v29, v29
	v_mul_f32_e32 v5, v31, v31
	v_fmac_f32_e32 v4, v28, v28
	v_fmac_f32_e32 v5, v30, v30
	v_add_f32_e32 v4, v4, v5
	v_add_f32_e32 v3, v3, v4
	v_mul_f32_e32 v4, v25, v25
	v_mul_f32_e32 v5, v27, v27
	v_fmac_f32_e32 v4, v24, v24
	v_fmac_f32_e32 v5, v26, v26
	v_add_f32_e32 v4, v4, v5
	v_add_f32_e32 v3, v4, v3
	v_mov_b32_e32 v0, v3
	s_nop 1
	v_permlane16_swap_b32_e32 v0, v3
	s_waitcnt lgkmcnt(0)
	v_add_f32_e32 v0, v3, v0
	v_mov_b32_e32 v2, v0
	s_nop 1
	v_permlane32_swap_b32_e32 v2, v0
	s_and_saveexec_b64 s[6:7], vcc
	s_cbranch_execz .LBB0_999
	s_waitcnt lgkmcnt(0)
	v_add_f32_e32 v0, v0, v2
	ds_write_b32 v1, v0 offset:2816
